# attention loop: stagger + collapsed row-max v_max triples and removed always-false alpha test (fewer VALU issue slots per step)
# speedup vs baseline: 1.0061x; 1.0061x over previous
; __device__ __forceinline__ void attn_unit(const unsigned char* __restrict__ CQt, const unsigned char* __restrict__ Wh, const f32x2* __restrict__ cst, const unsigned char* __restrict__ Kh, const unsigned char* __restrict__ Vh, bf16* __restrict__ Ob, char* lds) {
;     ...
;       if (s3 == 2) {
; #pragma unroll
;         for (int r = 0; r < 16; r += 2) { const f32x2 c0 = cc[r >> 1], c1 = cc[8 + (r >> 1)];
;           const float x0 = a0[r], y0 = a0[r + 1], x1 = a1[r], y1 = a1[r + 1];
;           a0[r] = x0 * c0.x - y0 * c0.y; a0[r + 1] = y0 * c0.x + x0 * c0.y; a1[r] = x1 * c1.x - y1 * c1.y; a1[r + 1] = y1 * c1.x + x1 * c1.y; } }
; #pragma unroll
;       for (int q = 0; q < 4; ++q) { int u0 = 0, u1 = 0;
;         u0 = __builtin_amdgcn_cvt_pk_fp8_f32(a0[4 * q] * QS, a0[4 * q + 1] * QS, u0, false); u0 = __builtin_amdgcn_cvt_pk_fp8_f32(a0[4 * q + 2] * QS, a0[4 * q + 3] * QS, u0, true);
;         u1 = __builtin_amdgcn_cvt_pk_fp8_f32(a1[4 * q] * QS, a1[4 * q + 1] * QS, u1, false); u1 = __builtin_amdgcn_cvt_pk_fp8_f32(a1[4 * q + 2] * QS, a1[4 * q + 3] * QS, u1, true);
;         qr[s3][q] = u0; qr[s3][4 + q] = u1; }
.LBB0_886:
	v_mul_f32_e32 v2, 0x3c553b94, v2
	v_mul_f32_e32 v3, 0x3c553b94, v3
	v_mov_b32_e32 v142, 0
	v_cvt_pk_fp8_f32 v142, v2, v3
	v_mul_f32_e32 v2, 0x3c553b94, v4
	v_mul_f32_e32 v3, 0x3c553b94, v5
	v_mov_b32_e32 v139, 0
	v_cvt_pk_fp8_f32 v142, v2, v3 op_sel:[0,0,1]
	v_mul_f32_e32 v2, 0x3c553b94, v22
	v_mul_f32_e32 v3, 0x3c553b94, v23
	v_cvt_pk_fp8_f32 v139, v2, v3
	v_mul_f32_e32 v4, 0x3c553b94, v6
	v_mul_f32_e32 v5, 0x3c553b94, v7
	v_mov_b32_e32 v143, 0
	v_cvt_pk_fp8_f32 v143, v4, v5
	v_mul_f32_e32 v2, 0x3c553b94, v24
	v_mul_f32_e32 v3, 0x3c553b94, v25
	v_cvt_pk_fp8_f32 v139, v2, v3 op_sel:[0,0,1]
	v_mul_f32_e32 v2, 0x3c553b94, v8
	v_mul_f32_e32 v3, 0x3c553b94, v9
	v_cvt_pk_fp8_f32 v143, v2, v3 op_sel:[0,0,1]
	v_mul_f32_e32 v2, 0x3c553b94, v26
	v_mul_f32_e32 v3, 0x3c553b94, v27
	v_mov_b32_e32 v140, 0
	v_cvt_pk_fp8_f32 v140, v2, v3
	v_mul_f32_e32 v4, 0x3c553b94, v10
	v_mul_f32_e32 v5, 0x3c553b94, v11
	v_mov_b32_e32 v144, 0
	v_cvt_pk_fp8_f32 v144, v4, v5
	v_mul_f32_e32 v2, 0x3c553b94, v28
	v_mul_f32_e32 v3, 0x3c553b94, v29
	v_cvt_pk_fp8_f32 v140, v2, v3 op_sel:[0,0,1]
	v_mul_f32_e32 v2, 0x3c553b94, v12
	v_mul_f32_e32 v3, 0x3c553b94, v13
	v_cvt_pk_fp8_f32 v144, v2, v3 op_sel:[0,0,1]
	v_mul_f32_e32 v2, 0x3c553b94, v30
	v_mul_f32_e32 v3, 0x3c553b94, v31
	v_mov_b32_e32 v141, 0
	v_cvt_pk_fp8_f32 v141, v2, v3
	v_mul_f32_e32 v4, 0x3c553b94, v14
	v_mul_f32_e32 v5, 0x3c553b94, v15
	v_mov_b32_e32 v145, 0
	v_cvt_pk_fp8_f32 v145, v4, v5
	v_mul_f32_e32 v2, 0x3c553b94, v32
	v_mul_f32_e32 v3, 0x3c553b94, v33
	v_cvt_pk_fp8_f32 v141, v2, v3 op_sel:[0,0,1]
	v_mul_f32_e32 v2, 0x3c553b94, v16
	v_mul_f32_e32 v3, 0x3c553b94, v17
	v_cvt_pk_fp8_f32 v145, v2, v3 op_sel:[0,0,1]
	v_mul_f32_e32 v2, 0x3c553b94, v50
	v_mul_f32_e32 v3, 0x3c553b94, v51
	v_mov_b32_e32 v146, 0
	v_cvt_pk_fp8_f32 v146, v2, v3
	v_mul_f32_e32 v4, 0x3c553b94, v34
	v_mul_f32_e32 v5, 0x3c553b94, v35
	v_mov_b32_e32 v150, 0
	v_cvt_pk_fp8_f32 v150, v4, v5
	v_mul_f32_e32 v2, 0x3c553b94, v52
	v_mul_f32_e32 v3, 0x3c553b94, v53
	v_cvt_pk_fp8_f32 v146, v2, v3 op_sel:[0,0,1]
	v_mul_f32_e32 v2, 0x3c553b94, v36
	v_mul_f32_e32 v3, 0x3c553b94, v37
	v_cvt_pk_fp8_f32 v150, v2, v3 op_sel:[0,0,1]
	v_mul_f32_e32 v2, 0x3c553b94, v54
	v_mul_f32_e32 v3, 0x3c553b94, v55
	v_mov_b32_e32 v147, 0
	v_cvt_pk_fp8_f32 v147, v2, v3
	v_mul_f32_e32 v4, 0x3c553b94, v38
	v_mul_f32_e32 v5, 0x3c553b94, v39
	v_mov_b32_e32 v151, 0
	v_cvt_pk_fp8_f32 v151, v4, v5
	v_mul_f32_e32 v2, 0x3c553b94, v56
	v_mul_f32_e32 v3, 0x3c553b94, v57
	v_cvt_pk_fp8_f32 v147, v2, v3 op_sel:[0,0,1]
	v_mul_f32_e32 v2, 0x3c553b94, v40
	v_mul_f32_e32 v3, 0x3c553b94, v41
	v_cvt_pk_fp8_f32 v151, v2, v3 op_sel:[0,0,1]
	v_mul_f32_e32 v2, 0x3c553b94, v58
	v_mul_f32_e32 v3, 0x3c553b94, v59
	v_mov_b32_e32 v148, 0
	v_cvt_pk_fp8_f32 v148, v2, v3
	v_mul_f32_e32 v4, 0x3c553b94, v42
	v_mul_f32_e32 v5, 0x3c553b94, v43
	v_mov_b32_e32 v152, 0
	v_cvt_pk_fp8_f32 v152, v4, v5
	v_mul_f32_e32 v2, 0x3c553b94, v60
	v_mul_f32_e32 v3, 0x3c553b94, v61
	v_cvt_pk_fp8_f32 v148, v2, v3 op_sel:[0,0,1]
	v_mul_f32_e32 v2, 0x3c553b94, v44
	v_mul_f32_e32 v3, 0x3c553b94, v45
	v_cvt_pk_fp8_f32 v152, v2, v3 op_sel:[0,0,1]
	v_mul_f32_e32 v2, 0x3c553b94, v62
	v_mul_f32_e32 v3, 0x3c553b94, v63
	v_mov_b32_e32 v149, 0
	v_cvt_pk_fp8_f32 v149, v2, v3
	v_mul_f32_e32 v4, 0x3c553b94, v46
	v_mul_f32_e32 v5, 0x3c553b94, v47
	v_mov_b32_e32 v153, 0
	v_cvt_pk_fp8_f32 v153, v4, v5
	v_mul_f32_e32 v2, 0x3c553b94, v64
	v_mul_f32_e32 v3, 0x3c553b94, v65
	v_cvt_pk_fp8_f32 v149, v2, v3 op_sel:[0,0,1]
	v_mul_f32_e32 v2, 0x3c553b94, v48
	v_mul_f32_e32 v3, 0x3c553b94, v49
	v_cvt_pk_fp8_f32 v153, v2, v3 op_sel:[0,0,1]
	s_waitcnt vmcnt(0)
	v_pk_mul_f32 v[2:3], v[134:135], v[82:83]
	v_mov_b32_e32 v154, 0
	v_sub_f32_e32 v4, v2, v3
	v_pk_mul_f32 v[2:3], v[134:135], v[82:83] op_sel:[0,1] op_sel_hi:[1,0]
	v_mov_b32_e32 v158, 0
	v_add_f32_e32 v5, v2, v3
	v_pk_mul_f32 v[2:3], v[136:137], v[84:85]
	s_mov_b32 m0, s88
	v_sub_f32_e32 v10, v2, v3
	v_pk_mul_f32 v[2:3], v[136:137], v[84:85] op_sel:[0,1] op_sel_hi:[1,0]
	v_or_b32_e32 v99, 1, v156
	v_add_f32_e32 v11, v2, v3
	v_pk_mul_f32 v[2:3], v[130:131], v[86:87]
	v_lshrrev_b32_e32 v65, 2, v189
	v_sub_f32_e32 v34, v2, v3
	v_pk_mul_f32 v[2:3], v[130:131], v[86:87] op_sel:[0,1] op_sel_hi:[1,0]
	v_mul_u32_u24_e32 v64, 0xc0, v170
	v_add_f32_e32 v35, v2, v3
	v_pk_mul_f32 v[2:3], v[132:133], v[88:89]
	v_mul_f32_e32 v18, 0x3c553b94, v18
	v_sub_f32_e32 v36, v2, v3
	v_pk_mul_f32 v[2:3], v[132:133], v[88:89] op_sel:[0,1] op_sel_hi:[1,0]
	v_mul_f32_e32 v19, 0x3c553b94, v19
	v_add_f32_e32 v37, v2, v3
	v_pk_mul_f32 v[2:3], v[126:127], v[90:91]
	v_mov_b32_e32 v138, 0
	v_sub_f32_e32 v50, v2, v3
	v_pk_mul_f32 v[2:3], v[126:127], v[90:91] op_sel:[0,1] op_sel_hi:[1,0]
	v_cvt_pk_fp8_f32 v138, v18, v19
	v_add_f32_e32 v51, v2, v3
	v_pk_mul_f32 v[2:3], v[128:129], v[92:93]
	v_mul_f32_e32 v18, 0x3c553b94, v20
	v_sub_f32_e32 v52, v2, v3
	v_pk_mul_f32 v[2:3], v[128:129], v[92:93] op_sel:[0,1] op_sel_hi:[1,0]
	v_mul_f32_e32 v19, 0x3c553b94, v21
	v_add_f32_e32 v53, v2, v3
	v_pk_mul_f32 v[2:3], v[122:123], v[94:95]
	v_cvt_pk_fp8_f32 v138, v18, v19 op_sel:[0,0,1]
	v_sub_f32_e32 v54, v2, v3
	v_pk_mul_f32 v[2:3], v[122:123], v[94:95] op_sel:[0,1] op_sel_hi:[1,0]
	v_mov_b32_e32 v155, 0
	v_add_f32_e32 v55, v2, v3
	v_pk_mul_f32 v[2:3], v[124:125], v[96:97]
	v_mov_b32_e32 v159, 0
	v_sub_f32_e32 v56, v2, v3
	v_pk_mul_f32 v[2:3], v[124:125], v[96:97] op_sel:[0,1] op_sel_hi:[1,0]
	v_or_b32_e32 v100, 4, v156
	v_add_f32_e32 v57, v2, v3
	v_pk_mul_f32 v[2:3], v[118:119], v[66:67]
	v_or_b32_e32 v101, 5, v156
	v_sub_f32_e32 v6, v2, v3
	v_pk_mul_f32 v[2:3], v[118:119], v[66:67] op_sel:[0,1] op_sel_hi:[1,0]
; __device__ __forceinline__ void qkt(f32x16& p0, f32x16& p1, const char* Ks, const v8i* qr, int r32, int hi, const f32x16& nm16) {
; #pragma unroll
;   for (int s = 0; s < 3; ++s) { const int c0 = 4 * s + 2 * hi;
;     const v8i a0 = __builtin_shufflevector(*reinterpret_cast<const v4i*>(Ks + k8_off(r32, c0)), *reinterpret_cast<const v4i*>(Ks + k8_off(r32, c0 + 1)), 0, 1, 2, 3, 4, 5, 6, 7);
;     const v8i a1 = __builtin_shufflevector(*reinterpret_cast<const v4i*>(Ks + 32 * DQK + k8_off(r32, c0)), *reinterpret_cast<const v4i*>(Ks + 32 * DQK + k8_off(r32, c0 + 1)), 0, 1, 2, 3, 4, 5, 6, 7);
;     p0 = __builtin_amdgcn_mfma_scale_f32_32x32x64_f8f6f4(a0, qr[s], s == 0 ? nm16 : p0, 0, 0, 0, 0, 0, 0);
;     p1 = __builtin_amdgcn_mfma_scale_f32_32x32x64_f8f6f4(a1, qr[s], s == 0 ? nm16 : p1, 0, 0, 0, 0, 0, 0); }
; }
; __device__ __forceinline__ void attn_unit(const unsigned char* __restrict__ CQt, const unsigned char* __restrict__ Wh, const f32x2* __restrict__ cst, const unsigned char* __restrict__ Kh, const unsigned char* __restrict__ Vh, bf16* __restrict__ Ob, char* lds) {
;     ...
;       if (s3 == 2) {
; #pragma unroll
;         for (int r = 0; r < 16; r += 2) { const f32x2 c0 = cc[r >> 1], c1 = cc[8 + (r >> 1)];
;           const float x0 = a0[r], y0 = a0[r + 1], x1 = a1[r], y1 = a1[r + 1];
;           a0[r] = x0 * c0.x - y0 * c0.y; a0[r + 1] = y0 * c0.x + x0 * c0.y; a1[r] = x1 * c1.x - y1 * c1.y; a1[r + 1] = y1 * c1.x + x1 * c1.y; } }
; #pragma unroll
;       for (int q = 0; q < 4; ++q) { int u0 = 0, u1 = 0;
;         u0 = __builtin_amdgcn_cvt_pk_fp8_f32(a0[4 * q] * QS, a0[4 * q + 1] * QS, u0, false); u0 = __builtin_amdgcn_cvt_pk_fp8_f32(a0[4 * q + 2] * QS, a0[4 * q + 3] * QS, u0, true);
;         u1 = __builtin_amdgcn_cvt_pk_fp8_f32(a1[4 * q] * QS, a1[4 * q + 1] * QS, u1, false); u1 = __builtin_amdgcn_cvt_pk_fp8_f32(a1[4 * q + 2] * QS, a1[4 * q + 3] * QS, u1, true);
;         qr[s3][q] = u0; qr[s3][4 + q] = u1; }
;     }
;     asm volatile("s_waitcnt lgkmcnt(0)" ::: "memory"); __builtin_amdgcn_s_barrier(); asm volatile("" ::: "memory");
;   }
;   ADMA(1, 1);
;   qkt(pA0, pA1, lds + KS(0), qr, r32, hi, nm16); partialSM<true>(pA0, pA1, m_reg, nm16, alA);
	v_mul_f32_e32 v6, 0x3c553b94, v6
	v_add_f32_e32 v7, v2, v3
	v_pk_mul_f32 v[2:3], v[120:121], v[68:69]
	v_mul_f32_e32 v7, 0x3c553b94, v7
	v_sub_f32_e32 v8, v2, v3
	v_pk_mul_f32 v[2:3], v[120:121], v[68:69] op_sel:[0,1] op_sel_hi:[1,0]
	v_cvt_pk_fp8_f32 v154, v6, v7
	v_add_f32_e32 v9, v2, v3
	v_pk_mul_f32 v[2:3], v[114:115], v[70:71]
	v_bitop3_b32 v6, v99, v65, 3 bitop3:0x78
	v_sub_f32_e32 v12, v2, v3
	v_pk_mul_f32 v[2:3], v[114:115], v[70:71] op_sel:[0,1] op_sel_hi:[1,0]
	v_lshlrev_b32_e32 v203, 4, v6
	v_add_f32_e32 v13, v2, v3
	v_pk_mul_f32 v[2:3], v[116:117], v[72:73]
	v_or_b32_e32 v6, v203, v64
	v_sub_f32_e32 v38, v2, v3
	v_pk_mul_f32 v[2:3], v[116:117], v[72:73] op_sel:[0,1] op_sel_hi:[1,0]
	v_add_u32_e32 v197, 0, v6
	v_add_f32_e32 v39, v2, v3
	v_pk_mul_f32 v[2:3], v[110:111], v[74:75]
	v_mul_f32_e32 v42, 0x3c553b94, v12
	v_sub_f32_e32 v40, v2, v3
	v_pk_mul_f32 v[2:3], v[110:111], v[74:75] op_sel:[0,1] op_sel_hi:[1,0]
	v_mul_f32_e32 v43, 0x3c553b94, v13
	v_add_f32_e32 v41, v2, v3
	v_pk_mul_f32 v[2:3], v[112:113], v[76:77]
	v_cvt_pk_fp8_f32 v155, v42, v43
	v_sub_f32_e32 v58, v2, v3
	v_pk_mul_f32 v[2:3], v[112:113], v[76:77] op_sel:[0,1] op_sel_hi:[1,0]
	v_or_b32_e32 v102, 8, v156
	v_add_f32_e32 v59, v2, v3
	v_pk_mul_f32 v[2:3], v[106:107], v[78:79]
	v_or_b32_e32 v103, 9, v156
	v_sub_f32_e32 v60, v2, v3
	v_pk_mul_f32 v[2:3], v[106:107], v[78:79] op_sel:[0,1] op_sel_hi:[1,0]
	v_mul_f32_e32 v10, 0x3c553b94, v10
	v_add_f32_e32 v61, v2, v3
	v_pk_mul_f32 v[2:3], v[108:109], v[80:81]
	v_mul_f32_e32 v11, 0x3c553b94, v11
	v_sub_f32_e32 v62, v2, v3
	v_pk_mul_f32 v[2:3], v[108:109], v[80:81] op_sel:[0,1] op_sel_hi:[1,0]
	v_mul_f32_e32 v50, 0x3c553b94, v50
	v_add_f32_e32 v63, v2, v3
	v_mul_f32_e32 v2, 0x3c553b94, v8
	v_mul_f32_e32 v3, 0x3c553b94, v9
	v_cvt_pk_fp8_f32 v154, v2, v3 op_sel:[0,0,1]
	v_mul_f32_e32 v2, 0x3c553b94, v4
	v_mul_f32_e32 v3, 0x3c553b94, v5
	v_cvt_pk_fp8_f32 v158, v2, v3
	v_lshl_add_u64 v[2:3], v[168:169], 0, 64
	global_load_lds_dwordx4 v[2:3], off
	v_bitop3_b32 v2, v156, v65, 3 bitop3:0x78
	v_lshlrev_b32_e32 v202, 4, v2
	v_or_b32_e32 v2, v202, v64
	v_add_u32_e32 v196, 0, v2
	ds_read_b128 v[2:5], v196 offset:8192
	ds_read_b128 v[6:9], v197 offset:8192
	s_waitcnt lgkmcnt(0)
	v_mfma_f32_32x32x64_f8f6f4 v[18:33], v[2:9], v[138:145], 0
	v_mul_f32_e32 v4, 0x3c553b94, v34
	v_mul_f32_e32 v5, 0x3c553b94, v35
	v_cvt_pk_fp8_f32 v159, v4, v5
	v_mul_f32_e32 v2, 0x3c553b94, v38
	v_mul_f32_e32 v3, 0x3c553b94, v39
	v_cvt_pk_fp8_f32 v155, v2, v3 op_sel:[0,0,1]
	v_mul_f32_e32 v2, 0x3c553b94, v36
	v_mul_f32_e32 v3, 0x3c553b94, v37
	v_cvt_pk_fp8_f32 v159, v2, v3 op_sel:[0,0,1]
	v_mul_f32_e32 v2, 0x3c553b94, v40
	v_mul_f32_e32 v3, 0x3c553b94, v41
	v_mov_b32_e32 v156, 0
	v_cvt_pk_fp8_f32 v156, v2, v3
	v_bitop3_b32 v2, v100, v65, 3 bitop3:0x78
	v_bitop3_b32 v6, v101, v65, 3 bitop3:0x78
	v_lshl_add_u32 v2, v2, 4, v64
	v_lshl_add_u32 v6, v6, 4, v64
	v_cvt_pk_fp8_f32 v158, v10, v11 op_sel:[0,0,1]
	ds_read_b128 v[10:13], v196 offset:14336
	ds_read_b128 v[14:17], v197 offset:14336
	v_add_u32_e32 v198, 0, v2
	v_add_u32_e32 v199, 0, v6
	ds_read_b128 v[2:5], v198 offset:8192
	ds_read_b128 v[6:9], v199 offset:8192
	s_waitcnt lgkmcnt(0)
	v_mfma_f32_32x32x64_f8f6f4 v[34:49], v[10:17], v[138:145], 0
	v_mul_f32_e32 v51, 0x3c553b94, v51
	v_mov_b32_e32 v160, 0
	v_cvt_pk_fp8_f32 v160, v50, v51
	v_mov_b32_e32 v157, 0
	v_mul_f32_e32 v10, 0x3c553b94, v58
	v_mul_f32_e32 v11, 0x3c553b94, v59
	v_mov_b32_e32 v161, 0
	v_cvt_pk_fp8_f32 v156, v10, v11 op_sel:[0,0,1]
	ds_read_b128 v[10:13], v198 offset:14336
	ds_read_b128 v[14:17], v199 offset:14336
	s_mov_b32 s9, s8
	s_mov_b32 s10, s8
	s_mov_b32 s11, s8
	s_mov_b32 s12, s8
	s_mov_b32 s13, s8
	s_mov_b32 s14, s8
	v_mfma_f32_32x32x64_f8f6f4 v[18:33], v[2:9], v[146:153], v[18:33]
	v_mul_f32_e32 v4, 0x3c553b94, v60
	v_mul_f32_e32 v5, 0x3c553b94, v61
	v_cvt_pk_fp8_f32 v157, v4, v5
	v_mul_f32_e32 v2, 0x3c553b94, v52
	v_mul_f32_e32 v3, 0x3c553b94, v53
	v_cvt_pk_fp8_f32 v160, v2, v3 op_sel:[0,0,1]
	v_mul_f32_e32 v2, 0x3c553b94, v62
	v_mul_f32_e32 v3, 0x3c553b94, v63
	v_cvt_pk_fp8_f32 v157, v2, v3 op_sel:[0,0,1]
	v_mul_f32_e32 v2, 0x3c553b94, v54
	v_mul_f32_e32 v3, 0x3c553b94, v55
	v_cvt_pk_fp8_f32 v161, v2, v3
	v_bitop3_b32 v2, v102, v65, 3 bitop3:0x78
	v_bitop3_b32 v6, v103, v65, 3 bitop3:0x78
	v_lshl_add_u32 v2, v2, 4, v64
	v_lshl_add_u32 v6, v6, 4, v64
	v_add_u32_e32 v200, 0, v2
	v_add_u32_e32 v201, 0, v6
	ds_read_b128 v[2:5], v200 offset:8192
	ds_read_b128 v[6:9], v201 offset:8192
	s_waitcnt lgkmcnt(0)
; #define AWAIT(n) asm volatile("s_waitcnt vmcnt(" #n ")" ::: "memory")
; #define ABAR() do { asm volatile("" ::: "memory"); __builtin_amdgcn_s_barrier(); asm volatile("" ::: "memory"); } while (0)
; template <bool FIRST>
; __device__ __forceinline__ void partialSM(f32x16& p0, f32x16& p1, float& m_reg, f32x16& nm16, float& alpha) {
;   float pmax = p0[0];
; #pragma unroll
;   for (int r = 1; r < 16; ++r) pmax = fmaxf(pmax, p0[r]);
; #pragma unroll
;   for (int r = 0; r < 16; ++r) pmax = fmaxf(pmax, p1[r]);
;   { auto rr = __builtin_amdgcn_permlane32_swap(__float_as_uint(pmax), __float_as_uint(pmax), false, false);
;     pmax = fmaxf(__uint_as_float(rr[0]), __uint_as_float(rr[1])); }
;   if (!FIRST && __builtin_expect(__all(pmax <= THR2), 1)) { alpha = 1.f; }
;   else { const float d = FIRST ? pmax : fmaxf(pmax, 0.f);
;     alpha = FIRST ? 1.f : __builtin_amdgcn_exp2f(-d); m_reg += d;
;     const float nm = -m_reg;
; #pragma unroll
;     for (int r = 0; r < 16; ++r) { p0[r] -= d; p1[r] -= d; float t = nm16[r]; asm volatile("v_mov_b32 %0, %1" : "+v"(t) : "v"(nm)); nm16[r] = t; } }
; #pragma unroll
;   for (int r = 0; r < 16; ++r) p0[r] = __builtin_amdgcn_exp2f(p0[r]);
; __device__ __forceinline__ void attn_unit(const unsigned char* __restrict__ CQt, const unsigned char* __restrict__ Wh, const f32x2* __restrict__ cst, const unsigned char* __restrict__ Kh, const unsigned char* __restrict__ Vh, bf16* __restrict__ Ob, char* lds) {
;     ...
; #pragma unroll
;       for (int q = 0; q < 4; ++q) { int u0 = 0, u1 = 0;
;         u0 = __builtin_amdgcn_cvt_pk_fp8_f32(a0[4 * q] * QS, a0[4 * q + 1] * QS, u0, false); u0 = __builtin_amdgcn_cvt_pk_fp8_f32(a0[4 * q + 2] * QS, a0[4 * q + 3] * QS, u0, true);
;         u1 = __builtin_amdgcn_cvt_pk_fp8_f32(a1[4 * q] * QS, a1[4 * q + 1] * QS, u1, false); u1 = __builtin_amdgcn_cvt_pk_fp8_f32(a1[4 * q + 2] * QS, a1[4 * q + 3] * QS, u1, true);
;         qr[s3][q] = u0; qr[s3][4 + q] = u1; }
;     }
;     asm volatile("s_waitcnt lgkmcnt(0)" ::: "memory"); __builtin_amdgcn_s_barrier(); asm volatile("" ::: "memory");
;   }
;   ADMA(1, 1);
;   qkt(pA0, pA1, lds + KS(0), qr, r32, hi, nm16); partialSM<true>(pA0, pA1, m_reg, nm16, alA);
;   AWAIT(0); ABAR();
	v_mfma_f32_32x32x64_f8f6f4 v[34:49], v[10:17], v[146:153], v[34:49]
	v_mul_f32_e32 v10, 0x3c553b94, v56
	v_mul_f32_e32 v11, 0x3c553b94, v57
	v_cvt_pk_fp8_f32 v161, v10, v11 op_sel:[0,0,1]
	ds_read_b128 v[50:53], v200 offset:14336
	ds_read_b128 v[54:57], v201 offset:14336
	s_mov_b32 s15, s8
	s_mov_b32 s16, s8
	s_mov_b32 s17, s8
	s_mov_b32 s18, s8
	s_mov_b32 s19, s8
	s_mov_b32 s20, s8
	s_mov_b32 s21, s8
	s_mov_b32 s22, s8
	s_mov_b32 s23, s8
	v_mov_b32_e32 v66, 0
	v_mov_b32_e32 v67, 0
	v_mfma_f32_32x32x64_f8f6f4 v[18:33], v[2:9], v[154:161], v[18:33]
	v_mov_b64_e32 v[2:3], s[8:9]
	v_mov_b64_e32 v[4:5], s[10:11]
	v_mov_b64_e32 v[6:7], s[12:13]
	v_mov_b64_e32 v[8:9], s[14:15]
	v_mov_b64_e32 v[10:11], s[16:17]
	v_mov_b64_e32 v[12:13], s[18:19]
	v_mov_b64_e32 v[14:15], s[20:21]
	v_mov_b64_e32 v[16:17], s[22:23]
	s_lshl_b32 s9, s33, 10
	s_and_b32 s9, s9, 0xffff0000
	v_mov_b32_e32 v68, 0
	v_mov_b32_e32 v69, 0
	v_mov_b32_e32 v70, 0
	v_mov_b32_e32 v71, 0
	v_mov_b32_e32 v72, 0
	s_waitcnt lgkmcnt(0)
	v_mfma_f32_32x32x64_f8f6f4 v[34:49], v[50:57], v[154:161], v[34:49]
	s_nop 2
	v_max_f32_e32 v50, v18, v19
	v_max3_f32 v50, v50, v20, v21
	v_max3_f32 v50, v50, v22, v23
	v_max3_f32 v50, v50, v24, v25
	v_max3_f32 v50, v50, v26, v27
	v_max3_f32 v50, v50, v28, v29
	v_max3_f32 v50, v50, v30, v31
	v_max3_f32 v50, v50, v32, v33
	v_mov_b32_e32 v73, 0
	v_mov_b32_e32 v74, 0
	v_mov_b32_e32 v75, 0
	v_mov_b32_e32 v76, 0
	v_mov_b32_e32 v77, 0
	s_nop 1
	v_max3_f32 v50, v50, v34, v35
	v_max3_f32 v50, v50, v36, v37
	v_max3_f32 v50, v50, v38, v39
	v_max3_f32 v50, v50, v40, v41
	v_max3_f32 v50, v50, v42, v43
	v_max3_f32 v50, v50, v44, v45
	v_max3_f32 v50, v50, v46, v47
	v_max3_f32 v50, v50, v48, v49
	v_mov_b32_e32 v51, v50
	s_nop 1
	v_permlane32_swap_b32_e32 v50, v51
	v_max_f32_e32 v50, v50, v51
	v_sub_f32_e32 v18, v18, v50
	v_add_f32_e32 v195, 0, v50
	v_sub_f32_e32 v19, v19, v50
	v_sub_f32_e32 v20, v20, v50
	v_sub_f32_e32 v21, v21, v50
	v_sub_f32_e32 v22, v22, v50
	v_sub_f32_e32 v23, v23, v50
	v_sub_f32_e32 v24, v24, v50
	v_sub_f32_e32 v25, v25, v50
	v_sub_f32_e32 v26, v26, v50
	v_sub_f32_e32 v27, v27, v50
	v_sub_f32_e32 v28, v28, v50
	v_sub_f32_e32 v29, v29, v50
	v_sub_f32_e32 v30, v30, v50
	v_mov_b32_e32 v78, 0
	v_sub_f32_e32 v31, v31, v50
	v_mov_b32_e32 v79, 0
	v_sub_f32_e32 v32, v32, v50
	v_mov_b32_e32 v80, 0
	v_sub_f32_e32 v33, v33, v50
	v_mov_b32_e32 v81, 0
	v_exp_f32_e32 v235, v18
	v_lshl_or_b32 v18, v171, 10, s9
	s_lshl_b32 s2, s2, 2
	v_xor_b32_e32 v51, 0x80000000, v195
	v_mov_b32 v66, v51
	v_mov_b32 v67, v51
	v_mov_b32 v68, v51
	v_mov_b32 v69, v51
	v_mov_b32 v70, v51
	v_mov_b32 v71, v51
	v_mov_b32 v72, v51
	v_mov_b32 v73, v51
	v_mov_b32 v74, v51
	v_mov_b32 v75, v51
	v_mov_b32 v76, v51
	v_mov_b32 v77, v51
	v_mov_b32 v78, v51
	v_mov_b32 v79, v51
	v_mov_b32 v80, v51
	v_mov_b32 v81, v51
	v_exp_f32_e32 v236, v19
	v_exp_f32_e32 v233, v20
	v_exp_f32_e32 v234, v21
	v_exp_f32_e32 v231, v22
	v_exp_f32_e32 v232, v23
	v_exp_f32_e32 v229, v24
	v_exp_f32_e32 v230, v25
	v_exp_f32_e32 v227, v26
	v_exp_f32_e32 v228, v27
	v_exp_f32_e32 v225, v28
	v_exp_f32_e32 v226, v29
	v_exp_f32_e32 v223, v30
	v_exp_f32_e32 v224, v31
	v_exp_f32_e32 v221, v32
	v_exp_f32_e32 v222, v33
	s_waitcnt vmcnt(0)
	v_and_or_b32 v18, v18, s84, v172
	s_add_i32 s93, s2, 0
	s_barrier
	v_ashrrev_i32_e32 v19, 31, v18
	v_lshlrev_b32_e32 v98, 4, v190
	v_mov_b32_e32 v162, 0
	v_sub_f32_e32 v97, v49, v50
	v_sub_f32_e32 v96, v48, v50
	v_sub_f32_e32 v95, v47, v50
	v_sub_f32_e32 v94, v46, v50
	v_sub_f32_e32 v93, v45, v50
	v_sub_f32_e32 v92, v44, v50
	v_sub_f32_e32 v91, v43, v50
	v_sub_f32_e32 v90, v42, v50
	v_sub_f32_e32 v89, v41, v50
	v_sub_f32_e32 v88, v40, v50
	v_sub_f32_e32 v87, v39, v50
	v_sub_f32_e32 v86, v38, v50
	v_sub_f32_e32 v85, v37, v50
	v_sub_f32_e32 v84, v36, v50
	v_sub_f32_e32 v83, v35, v50
	v_sub_f32_e32 v82, v34, v50
	v_lshl_add_u32 v204, v170, 6, 0
	v_cmp_gt_u32_e64 s[2:3], 32, v171
	v_lshl_add_u32 v192, v170, 2, s93
	v_lshl_add_u64 v[170:171], s[66:67], 0, v[18:19]
	v_mov_b64_e32 v[64:65], v[16:17]
	v_mov_b64_e32 v[48:49], v[16:17]
	v_mov_b64_e32 v[32:33], v[16:17]
	v_add_u32_e32 v191, s93, v98
	v_lshl_add_u64 v[172:173], v[166:167], 0, s[4:5]
	v_lshl_add_u64 v[174:175], s[4:5], 0, v[164:165]
	s_add_u32 s24, s0, 0x6000
	s_addc_u32 s25, s1, 0
	s_add_u32 s26, s6, 0x4e000040
	s_addc_u32 s27, s7, 0
	s_and_b32 s94, s64, 1
	s_cmp_eq_u32 s94, 0
	s_cbranch_scc0 .Lstg_pre_l0
	s_mov_b32 m0, s90
	s_nop 0
	global_load_lds_dwordx4 v164, s[24:25]
	s_mov_b32 m0, s88
	s_nop 0
	global_load_lds_dwordx4 v170, s[26:27]
	s_add_u32 s24, s24, 0x3000
	s_addc_u32 s25, s25, 0
	s_add_u32 s26, s26, 64
	s_addc_u32 s27, s27, 0

; template <bool FIRST>
; __device__ __forceinline__ void partialSM(f32x16& p0, f32x16& p1, float& m_reg, f32x16& nm16, float& alpha) {
;   float pmax = p0[0];
; #pragma unroll
;   for (int r = 1; r < 16; ++r) pmax = fmaxf(pmax, p0[r]);
; #pragma unroll
;   for (int r = 0; r < 16; ++r) pmax = fmaxf(pmax, p1[r]);
;   { auto rr = __builtin_amdgcn_permlane32_swap(__float_as_uint(pmax), __float_as_uint(pmax), false, false);
;     pmax = fmaxf(__uint_as_float(rr[0]), __uint_as_float(rr[1])); }
;   if (!FIRST && __builtin_expect(__all(pmax <= THR2), 1)) { alpha = 1.f; }
; __device__ __forceinline__ void pv_d0(f32x16* o, const char* Vs, v8i pa, int r32, int hi) {
; #pragma unroll
;   for (int d0 = 0; d0 < 4; ++d0) { const int row = 32 * d0 + r32, x = (row >> 2) & 3;
;     const v8i vb = __builtin_shufflevector(*reinterpret_cast<const v4i*>(Vs + row * 64 + (((2 * hi) ^ x) << 4)), *reinterpret_cast<const v4i*>(Vs + row * 64 + (((2 * hi + 1) ^ x) << 4)), 0, 1, 2, 3, 4, 5, 6, 7);
;     o[d0] = __builtin_amdgcn_mfma_scale_f32_32x32x64_f8f6f4(pa, vb, o[d0], 0, 0, 0, 0, 0, 0); }
; }
.Lstg_mid0_l0:
	v_add_u32_e32 v194, v204, v203
	v_add_u32_e32 v193, v204, v202
	ds_read_b128 v[86:89], v194
	ds_read_b128 v[82:85], v193
	ds_read_b128 v[90:93], v193 offset:2048
	ds_read_b128 v[94:97], v194 offset:2048
	s_nop 4
	v_max_f32_e32 v182, v114, v115
	v_max_f32_e32 v183, v114, v114
	s_waitcnt lgkmcnt(0)
	v_mfma_f32_32x32x64_f8f6f4 v[2:17], v[130:137], v[82:89], v[2:17]
	v_max3_f32 v182, v182, v116, v117
	v_max3_f32 v182, v182, v118, v119
	v_max3_f32 v182, v182, v120, v121
	v_max3_f32 v182, v182, v122, v123
	v_max3_f32 v182, v182, v124, v125
	v_max3_f32 v182, v182, v126, v127
	v_max3_f32 v182, v182, v128, v129
	v_max3_f32 v182, v182, v98, v99
	v_mov_b32_e32 v208, 1.0
	v_mfma_f32_32x32x64_f8f6f4 v[50:65], v[130:137], v[90:97], v[50:65]
	ds_read_b128 v[82:85], v193 offset:4096
	ds_read_b128 v[90:93], v193 offset:6144
	ds_read_b128 v[86:89], v194 offset:4096
	ds_read_b128 v[94:97], v194 offset:6144
	s_waitcnt lgkmcnt(0)
	v_mfma_f32_32x32x64_f8f6f4 v[34:49], v[130:137], v[82:89], v[34:49]
	v_max3_f32 v82, v182, v100, v101
	v_max3_f32 v82, v82, v102, v103
	v_max3_f32 v82, v82, v104, v105
	v_max3_f32 v82, v82, v106, v107
	v_max3_f32 v82, v82, v108, v109
	v_max3_f32 v82, v82, v110, v111
	v_max3_f32 v82, v82, v112, v113
	v_mov_b32_e32 v83, v82
	s_nop 1
	v_permlane32_swap_b32_e32 v82, v83
	v_max_f32_e32 v82, v82, v83
	v_cmp_ge_f32_e32 vcc, s85, v82
	s_cmp_eq_u64 vcc, exec
	v_mfma_f32_32x32x64_f8f6f4 v[18:33], v[130:137], v[90:97], v[18:33]
	s_cbranch_scc0 .LBB0_931
	s_branch .LBB0_894

; template <bool FIRST>
; __device__ __forceinline__ void partialSM(f32x16& p0, f32x16& p1, float& m_reg, f32x16& nm16, float& alpha) {
;   float pmax = p0[0];
; #pragma unroll
;   for (int r = 1; r < 16; ++r) pmax = fmaxf(pmax, p0[r]);
; #pragma unroll
;   for (int r = 0; r < 16; ++r) pmax = fmaxf(pmax, p1[r]);
;   { auto rr = __builtin_amdgcn_permlane32_swap(__float_as_uint(pmax), __float_as_uint(pmax), false, false);
;     pmax = fmaxf(__uint_as_float(rr[0]), __uint_as_float(rr[1])); }
;   if (!FIRST && __builtin_expect(__all(pmax <= THR2), 1)) { alpha = 1.f; }
; __device__ __forceinline__ void pv_d0(f32x16* o, const char* Vs, v8i pa, int r32, int hi) {
; #pragma unroll
;   for (int d0 = 0; d0 < 4; ++d0) { const int row = 32 * d0 + r32, x = (row >> 2) & 3;
;     const v8i vb = __builtin_shufflevector(*reinterpret_cast<const v4i*>(Vs + row * 64 + (((2 * hi) ^ x) << 4)), *reinterpret_cast<const v4i*>(Vs + row * 64 + (((2 * hi + 1) ^ x) << 4)), 0, 1, 2, 3, 4, 5, 6, 7);
;     o[d0] = __builtin_amdgcn_mfma_scale_f32_32x32x64_f8f6f4(pa, vb, o[d0], 0, 0, 0, 0, 0, 0); }
; }
.Lstg_mid1_l0:
	ds_read_b128 v[102:105], v194 offset:32768
	ds_read_b128 v[98:101], v193 offset:32768
	ds_read_b128 v[106:109], v193 offset:34816
	ds_read_b128 v[110:113], v194 offset:34816
	s_nop 6
	v_max_f32_e32 v182, v114, v115
	v_max_f32_e32 v183, v114, v114
	s_waitcnt lgkmcnt(0)
	v_mfma_f32_32x32x64_f8f6f4 v[2:17], v[130:137], v[98:105], v[2:17]
	v_max3_f32 v182, v182, v116, v117
	v_max3_f32 v182, v182, v118, v119
	v_max3_f32 v182, v182, v120, v121
	v_max3_f32 v182, v182, v122, v123
	v_max3_f32 v182, v182, v124, v125
	v_max3_f32 v182, v182, v126, v127
	v_max3_f32 v182, v182, v128, v129
	v_max3_f32 v182, v182, v82, v83
	v_mov_b32_e32 v211, 1.0
	v_mfma_f32_32x32x64_f8f6f4 v[50:65], v[130:137], v[106:113], v[50:65]
	ds_read_b128 v[98:101], v193 offset:36864
	ds_read_b128 v[106:109], v193 offset:38912
	ds_read_b128 v[102:105], v194 offset:36864
	ds_read_b128 v[110:113], v194 offset:38912
	s_waitcnt lgkmcnt(0)
	v_mfma_f32_32x32x64_f8f6f4 v[34:49], v[130:137], v[98:105], v[34:49]
	v_max3_f32 v98, v182, v84, v85
	v_max3_f32 v98, v98, v86, v87
	v_max3_f32 v98, v98, v88, v89
	v_max3_f32 v98, v98, v90, v91
	v_max3_f32 v98, v98, v92, v93
	v_max3_f32 v98, v98, v94, v95
	v_max3_f32 v98, v98, v96, v97
	v_mov_b32_e32 v99, v98
	s_nop 1
	v_permlane32_swap_b32_e32 v98, v99
	v_max_f32_e32 v98, v98, v99
	v_cmp_ge_f32_e32 vcc, s85, v98
	s_cmp_eq_u64 vcc, exec
	v_mfma_f32_32x32x64_f8f6f4 v[18:33], v[130:137], v[106:113], v[18:33]
	s_cbranch_scc0 .LBB0_932
	s_branch .LBB0_901

; template <bool FIRST>
; __device__ __forceinline__ void partialSM(f32x16& p0, f32x16& p1, float& m_reg, f32x16& nm16, float& alpha) {
;   float pmax = p0[0];
; #pragma unroll
;   for (int r = 1; r < 16; ++r) pmax = fmaxf(pmax, p0[r]);
; #pragma unroll
;   for (int r = 0; r < 16; ++r) pmax = fmaxf(pmax, p1[r]);
;   { auto rr = __builtin_amdgcn_permlane32_swap(__float_as_uint(pmax), __float_as_uint(pmax), false, false);
;     pmax = fmaxf(__uint_as_float(rr[0]), __uint_as_float(rr[1])); }
;   if (!FIRST && __builtin_expect(__all(pmax <= THR2), 1)) { alpha = 1.f; }
; __device__ __forceinline__ void pv_d0(f32x16* o, const char* Vs, v8i pa, int r32, int hi) {
; #pragma unroll
;   for (int d0 = 0; d0 < 4; ++d0) { const int row = 32 * d0 + r32, x = (row >> 2) & 3;
;     const v8i vb = __builtin_shufflevector(*reinterpret_cast<const v4i*>(Vs + row * 64 + (((2 * hi) ^ x) << 4)), *reinterpret_cast<const v4i*>(Vs + row * 64 + (((2 * hi + 1) ^ x) << 4)), 0, 1, 2, 3, 4, 5, 6, 7);
;     o[d0] = __builtin_amdgcn_mfma_scale_f32_32x32x64_f8f6f4(pa, vb, o[d0], 0, 0, 0, 0, 0, 0); }
; }
.Lstg_mid2_l0:
	ds_read_b128 v[86:89], v194 offset:40960
	ds_read_b128 v[82:85], v193 offset:40960
	ds_read_b128 v[90:93], v193 offset:43008
	ds_read_b128 v[94:97], v194 offset:43008
	v_max_f32_e32 v182, v114, v115
	v_max_f32_e32 v183, v114, v114
	s_waitcnt lgkmcnt(0)
	v_mfma_f32_32x32x64_f8f6f4 v[2:17], v[130:137], v[82:89], v[2:17]
	v_max3_f32 v182, v182, v116, v117
	v_max3_f32 v182, v182, v118, v119
	v_max3_f32 v182, v182, v120, v121
	v_max3_f32 v182, v182, v122, v123
	v_max3_f32 v182, v182, v124, v125
	v_max3_f32 v182, v182, v126, v127
	v_max3_f32 v182, v182, v128, v129
	v_max3_f32 v182, v182, v98, v99
	v_mov_b32_e32 v214, 1.0
	v_mfma_f32_32x32x64_f8f6f4 v[50:65], v[130:137], v[90:97], v[50:65]
	ds_read_b128 v[82:85], v193 offset:45056
	ds_read_b128 v[90:93], v193 offset:47104
	ds_read_b128 v[86:89], v194 offset:45056
	ds_read_b128 v[94:97], v194 offset:47104
	s_waitcnt lgkmcnt(0)
	v_mfma_f32_32x32x64_f8f6f4 v[34:49], v[130:137], v[82:89], v[34:49]
	v_max3_f32 v82, v182, v100, v101
	v_max3_f32 v82, v82, v102, v103
	v_max3_f32 v82, v82, v104, v105
	v_max3_f32 v82, v82, v106, v107
	v_max3_f32 v82, v82, v108, v109
	v_max3_f32 v82, v82, v110, v111
	v_max3_f32 v82, v82, v112, v113
	v_mov_b32_e32 v83, v82
	s_nop 1
	v_permlane32_swap_b32_e32 v82, v83
	v_max_f32_e32 v82, v82, v83
	v_cmp_ge_f32_e32 vcc, s85, v82
	s_cmp_eq_u64 vcc, exec
	v_mfma_f32_32x32x64_f8f6f4 v[18:33], v[130:137], v[90:97], v[18:33]
	s_cbranch_scc0 .LBB0_933
	s_branch .LBB0_908

; template <bool FIRST>
; __device__ __forceinline__ void partialSM(f32x16& p0, f32x16& p1, float& m_reg, f32x16& nm16, float& alpha) {
;   float pmax = p0[0];
; #pragma unroll
;   for (int r = 1; r < 16; ++r) pmax = fmaxf(pmax, p0[r]);
; #pragma unroll
;   for (int r = 0; r < 16; ++r) pmax = fmaxf(pmax, p1[r]);
;   { auto rr = __builtin_amdgcn_permlane32_swap(__float_as_uint(pmax), __float_as_uint(pmax), false, false);
;     pmax = fmaxf(__uint_as_float(rr[0]), __uint_as_float(rr[1])); }
;   if (!FIRST && __builtin_expect(__all(pmax <= THR2), 1)) { alpha = 1.f; }
; __device__ __forceinline__ void pv_d0(f32x16* o, const char* Vs, v8i pa, int r32, int hi) {
; #pragma unroll
;   for (int d0 = 0; d0 < 4; ++d0) { const int row = 32 * d0 + r32, x = (row >> 2) & 3;
;     const v8i vb = __builtin_shufflevector(*reinterpret_cast<const v4i*>(Vs + row * 64 + (((2 * hi) ^ x) << 4)), *reinterpret_cast<const v4i*>(Vs + row * 64 + (((2 * hi + 1) ^ x) << 4)), 0, 1, 2, 3, 4, 5, 6, 7);
;     o[d0] = __builtin_amdgcn_mfma_scale_f32_32x32x64_f8f6f4(pa, vb, o[d0], 0, 0, 0, 0, 0, 0); }
; }
.Lstg_mid3_l0:
	ds_read_b128 v[102:105], v194
	ds_read_b128 v[98:101], v193
	ds_read_b128 v[106:109], v193 offset:2048
	ds_read_b128 v[110:113], v194 offset:2048
	s_nop 6
	v_max_f32_e32 v182, v114, v115
	v_max_f32_e32 v183, v114, v114
	s_waitcnt lgkmcnt(0)
	v_mfma_f32_32x32x64_f8f6f4 v[2:17], v[130:137], v[98:105], v[2:17]
	v_max3_f32 v182, v182, v116, v117
	v_max3_f32 v182, v182, v118, v119
	v_max3_f32 v182, v182, v120, v121
	v_max3_f32 v182, v182, v122, v123
	v_max3_f32 v182, v182, v124, v125
	v_max3_f32 v182, v182, v126, v127
	v_max3_f32 v182, v182, v128, v129
	v_max3_f32 v182, v182, v82, v83
	v_mov_b32_e32 v217, 1.0
	v_mfma_f32_32x32x64_f8f6f4 v[50:65], v[130:137], v[106:113], v[50:65]
	ds_read_b128 v[98:101], v193 offset:4096
	ds_read_b128 v[106:109], v193 offset:6144
	ds_read_b128 v[102:105], v194 offset:4096
	ds_read_b128 v[110:113], v194 offset:6144
	s_waitcnt lgkmcnt(0)
	v_mfma_f32_32x32x64_f8f6f4 v[34:49], v[130:137], v[98:105], v[34:49]
	v_max3_f32 v98, v182, v84, v85
	v_max3_f32 v98, v98, v86, v87
	v_max3_f32 v98, v98, v88, v89
	v_max3_f32 v98, v98, v90, v91
	v_max3_f32 v98, v98, v92, v93
	v_max3_f32 v98, v98, v94, v95
	v_max3_f32 v98, v98, v96, v97
	v_mov_b32_e32 v99, v98
	s_nop 1
	v_permlane32_swap_b32_e32 v98, v99
	v_max_f32_e32 v98, v98, v99
	v_cmp_ge_f32_e32 vcc, s85, v98
	s_cmp_eq_u64 vcc, exec
	v_mfma_f32_32x32x64_f8f6f4 v[18:33], v[130:137], v[106:113], v[18:33]
	s_cbranch_scc0 .LBB0_934
	s_branch .LBB0_915

; template <bool FIRST>
; __device__ __forceinline__ void partialSM(f32x16& p0, f32x16& p1, float& m_reg, f32x16& nm16, float& alpha) {
;   float pmax = p0[0];
; #pragma unroll
;   for (int r = 1; r < 16; ++r) pmax = fmaxf(pmax, p0[r]);
; #pragma unroll
;   for (int r = 0; r < 16; ++r) pmax = fmaxf(pmax, p1[r]);
;   { auto rr = __builtin_amdgcn_permlane32_swap(__float_as_uint(pmax), __float_as_uint(pmax), false, false);
;     pmax = fmaxf(__uint_as_float(rr[0]), __uint_as_float(rr[1])); }
;   if (!FIRST && __builtin_expect(__all(pmax <= THR2), 1)) { alpha = 1.f; }
; __device__ __forceinline__ void pv_d0(f32x16* o, const char* Vs, v8i pa, int r32, int hi) {
; #pragma unroll
;   for (int d0 = 0; d0 < 4; ++d0) { const int row = 32 * d0 + r32, x = (row >> 2) & 3;
;     const v8i vb = __builtin_shufflevector(*reinterpret_cast<const v4i*>(Vs + row * 64 + (((2 * hi) ^ x) << 4)), *reinterpret_cast<const v4i*>(Vs + row * 64 + (((2 * hi + 1) ^ x) << 4)), 0, 1, 2, 3, 4, 5, 6, 7);
;     o[d0] = __builtin_amdgcn_mfma_scale_f32_32x32x64_f8f6f4(pa, vb, o[d0], 0, 0, 0, 0, 0, 0); }
; }
.Lstg_mid4_l0:
	ds_read_b128 v[86:89], v194 offset:32768
	ds_read_b128 v[82:85], v193 offset:32768
	ds_read_b128 v[90:93], v193 offset:34816
	ds_read_b128 v[94:97], v194 offset:34816
	v_max_f32_e32 v182, v114, v115
	v_max_f32_e32 v183, v114, v114
	s_waitcnt lgkmcnt(0)
	v_mfma_f32_32x32x64_f8f6f4 v[2:17], v[130:137], v[82:89], v[2:17]
	v_max3_f32 v182, v182, v116, v117
	v_max3_f32 v182, v182, v118, v119
	v_max3_f32 v182, v182, v120, v121
	v_max3_f32 v182, v182, v122, v123
	v_max3_f32 v182, v182, v124, v125
	v_max3_f32 v182, v182, v126, v127
	v_max3_f32 v182, v182, v128, v129
	v_max3_f32 v182, v182, v98, v99
	v_mov_b32_e32 v220, 1.0
	v_mfma_f32_32x32x64_f8f6f4 v[50:65], v[130:137], v[90:97], v[50:65]
	ds_read_b128 v[82:85], v193 offset:36864
	ds_read_b128 v[90:93], v193 offset:38912
	ds_read_b128 v[86:89], v194 offset:36864
	ds_read_b128 v[94:97], v194 offset:38912
	s_waitcnt lgkmcnt(0)
	v_mfma_f32_32x32x64_f8f6f4 v[34:49], v[130:137], v[82:89], v[34:49]
	v_max3_f32 v82, v182, v100, v101
	v_max3_f32 v82, v82, v102, v103
	v_max3_f32 v82, v82, v104, v105
	v_max3_f32 v82, v82, v106, v107
	v_max3_f32 v82, v82, v108, v109
	v_max3_f32 v82, v82, v110, v111
	v_max3_f32 v82, v82, v112, v113
	v_mov_b32_e32 v83, v82
	s_nop 1
	v_permlane32_swap_b32_e32 v82, v83
	v_max_f32_e32 v82, v82, v83
	v_cmp_ge_f32_e32 vcc, s85, v82
	s_cmp_eq_u64 vcc, exec
	v_mfma_f32_32x32x64_f8f6f4 v[18:33], v[130:137], v[90:97], v[18:33]
	s_cbranch_scc0 .LBB0_935
	s_branch .LBB0_922

; template <bool FIRST>
; __device__ __forceinline__ void partialSM(f32x16& p0, f32x16& p1, float& m_reg, f32x16& nm16, float& alpha) {
;   float pmax = p0[0];
; #pragma unroll
;   for (int r = 1; r < 16; ++r) pmax = fmaxf(pmax, p0[r]);
; #pragma unroll
;   for (int r = 0; r < 16; ++r) pmax = fmaxf(pmax, p1[r]);
;   { auto rr = __builtin_amdgcn_permlane32_swap(__float_as_uint(pmax), __float_as_uint(pmax), false, false);
;     pmax = fmaxf(__uint_as_float(rr[0]), __uint_as_float(rr[1])); }
;   if (!FIRST && __builtin_expect(__all(pmax <= THR2), 1)) { alpha = 1.f; }
; __device__ __forceinline__ void pv_d0(f32x16* o, const char* Vs, v8i pa, int r32, int hi) {
; #pragma unroll
;   for (int d0 = 0; d0 < 4; ++d0) { const int row = 32 * d0 + r32, x = (row >> 2) & 3;
;     const v8i vb = __builtin_shufflevector(*reinterpret_cast<const v4i*>(Vs + row * 64 + (((2 * hi) ^ x) << 4)), *reinterpret_cast<const v4i*>(Vs + row * 64 + (((2 * hi + 1) ^ x) << 4)), 0, 1, 2, 3, 4, 5, 6, 7);
;     o[d0] = __builtin_amdgcn_mfma_scale_f32_32x32x64_f8f6f4(pa, vb, o[d0], 0, 0, 0, 0, 0, 0); }
; }
.Lstg_mid5_l0:
	ds_read_b128 v[104:107], v194 offset:40960
	ds_read_b128 v[100:103], v193 offset:40960
	ds_read_b128 v[222:225], v193 offset:43008
	ds_read_b128 v[226:229], v194 offset:43008
	v_max_f32_e32 v108, v114, v115
	v_max_f32_e32 v109, v114, v114
	s_waitcnt lgkmcnt(0)
	v_mfma_f32_32x32x64_f8f6f4 v[2:17], v[130:137], v[100:107], v[2:17]
	v_max3_f32 v108, v108, v116, v117
	v_max3_f32 v108, v108, v118, v119
	v_max3_f32 v108, v108, v120, v121
	v_max3_f32 v108, v108, v122, v123
	v_max3_f32 v108, v108, v124, v125
	v_max3_f32 v108, v108, v126, v127
	v_max3_f32 v108, v108, v128, v129
	v_max3_f32 v108, v108, v82, v83
	v_mov_b32_e32 v176, 1.0
	v_mfma_f32_32x32x64_f8f6f4 v[50:65], v[130:137], v[222:229], v[50:65]
	ds_read_b128 v[100:103], v193 offset:45056
	ds_read_b128 v[222:225], v193 offset:47104
	ds_read_b128 v[104:107], v194 offset:45056
	ds_read_b128 v[226:229], v194 offset:47104
	s_waitcnt lgkmcnt(0)
	v_mfma_f32_32x32x64_f8f6f4 v[34:49], v[130:137], v[100:107], v[34:49]
	v_max3_f32 v100, v108, v84, v85
	v_max3_f32 v100, v100, v86, v87
	v_max3_f32 v100, v100, v88, v89
	v_max3_f32 v100, v100, v90, v91
	v_max3_f32 v100, v100, v92, v93
	v_max3_f32 v100, v100, v94, v95
	v_max3_f32 v100, v100, v96, v97
	v_mov_b32_e32 v101, v100
	s_nop 1
	v_permlane32_swap_b32_e32 v100, v101
	v_max_f32_e32 v100, v100, v101
	v_cmp_ge_f32_e32 vcc, s85, v100
	s_cmp_eq_u64 vcc, exec
	v_mfma_f32_32x32x64_f8f6f4 v[18:33], v[130:137], v[222:229], v[18:33]
	s_cbranch_scc0 .LBB0_936
	s_branch .LBB0_929

; template <bool FIRST>
; __device__ __forceinline__ void partialSM(f32x16& p0, f32x16& p1, float& m_reg, f32x16& nm16, float& alpha) {
;   float pmax = p0[0];
; #pragma unroll
;   for (int r = 1; r < 16; ++r) pmax = fmaxf(pmax, p0[r]);
; #pragma unroll
;   for (int r = 0; r < 16; ++r) pmax = fmaxf(pmax, p1[r]);
;   { auto rr = __builtin_amdgcn_permlane32_swap(__float_as_uint(pmax), __float_as_uint(pmax), false, false);
;     pmax = fmaxf(__uint_as_float(rr[0]), __uint_as_float(rr[1])); }
;   if (!FIRST && __builtin_expect(__all(pmax <= THR2), 1)) { alpha = 1.f; }
;   else { const float d = FIRST ? pmax : fmaxf(pmax, 0.f);
;     alpha = FIRST ? 1.f : __builtin_amdgcn_exp2f(-d); m_reg += d;
;     const float nm = -m_reg;
; #pragma unroll
;     for (int r = 0; r < 16; ++r) { p0[r] -= d; p1[r] -= d; float t = nm16[r]; asm volatile("v_mov_b32 %0, %1" : "+v"(t) : "v"(nm)); nm16[r] = t; } }
; #pragma unroll
;   for (int r = 0; r < 16; ++r) p0[r] = __builtin_amdgcn_exp2f(p0[r]);
; }
; __device__ __forceinline__ void finishSM(f32x16& p0, f32x16& p1, float alpha, float& l_reg, v8i& pa) {
; #pragma unroll
;   for (int r = 0; r < 16; ++r) p1[r] = __builtin_amdgcn_exp2f(p1[r]);
;   float ps = 0;
; #pragma unroll
;   for (int r = 0; r < 16; ++r) ps += p0[r];
; #pragma unroll
;   for (int r = 0; r < 16; ++r) ps += p1[r];
;   { auto rr = __builtin_amdgcn_permlane32_swap(__float_as_uint(ps), __float_as_uint(ps), false, false);
;     ps = __uint_as_float(rr[0]) + __uint_as_float(rr[1]); }
;   l_reg = l_reg * alpha + ps;
; #pragma unroll
;   for (int q = 0; q < 4; ++q) { int w0 = pa[q], w1 = pa[4 + q];
;     w0 = __builtin_amdgcn_cvt_pk_fp8_f32(p0[4 * q], p0[4 * q + 1], w0, false); w0 = __builtin_amdgcn_cvt_pk_fp8_f32(p0[4 * q + 2], p0[4 * q + 3], w0, true);
;     w1 = __builtin_amdgcn_cvt_pk_fp8_f32(p1[4 * q], p1[4 * q + 1], w1, false); w1 = __builtin_amdgcn_cvt_pk_fp8_f32(p1[4 * q + 2], p1[4 * q + 3], w1, true);
;     pa[q] = w0; pa[4 + q] = w1; }
; }
; __device__ __forceinline__ void qkt(f32x16& p0, f32x16& p1, const char* Ks, const v8i* qr, int r32, int hi, const f32x16& nm16) {
; #pragma unroll
;   for (int s = 0; s < 3; ++s) { const int c0 = 4 * s + 2 * hi;
;     const v8i a0 = __builtin_shufflevector(*reinterpret_cast<const v4i*>(Ks + k8_off(r32, c0)), *reinterpret_cast<const v4i*>(Ks + k8_off(r32, c0 + 1)), 0, 1, 2, 3, 4, 5, 6, 7);
.LBB0_939:
	v_lshl_add_u64 v[98:99], v[168:169], 0, s[56:57]
	s_mov_b32 m0, s89
	s_nop 0
	global_load_lds_dwordx4 v[98:99], off
	s_mov_b32 m0, s88
	s_nop 0
	global_load_lds_dwordx4 v170, s[26:27]
	ds_read_b128 v[102:105], v197 offset:20480
	ds_read_b128 v[98:101], v196 offset:20480
	ds_read_b128 v[202:205], v196 offset:26624
	ds_read_b128 v[206:209], v197 offset:26624
	v_add_f32_e32 v170, 0, v235
	ds_read_b128 v[210:213], v198 offset:20480
	ds_read_b128 v[238:241], v198 offset:26624
	ds_read_b128 v[214:217], v199 offset:20480
	ds_read_b128 v[242:245], v199 offset:26624
	ds_read_b128 v[246:249], v200 offset:20480
	ds_read_b128 v[178:181], v200 offset:26624
	ds_read_b128 v[250:253], v201 offset:20480
	ds_read_b128 v[182:185], v201 offset:26624
	s_waitcnt lgkmcnt(0)
	v_mfma_f32_32x32x64_f8f6f4 v[114:129], v[98:105], v[138:145], v[66:81]
	v_add_f32_e32 v170, v236, v170
	v_add_f32_e32 v170, v233, v170
	v_add_f32_e32 v170, v234, v170
	v_add_f32_e32 v170, v231, v170
	v_add_f32_e32 v170, v232, v170
	v_add_f32_e32 v170, v229, v170
	v_add_f32_e32 v170, v230, v170
	v_add_f32_e32 v170, v227, v170
	v_add_f32_e32 v170, v228, v170
	v_add_f32_e32 v170, v225, v170
	v_add_f32_e32 v170, v226, v170
	v_exp_f32_e32 v82, v82
	v_add_f32_e32 v170, v223, v170
	v_exp_f32_e32 v83, v83
	v_add_f32_e32 v170, v224, v170
	v_mfma_f32_32x32x64_f8f6f4 v[98:113], v[202:209], v[138:145], v[66:81]
	v_exp_f32_e32 v84, v84
	v_add_f32_e32 v170, v221, v170
	v_exp_f32_e32 v85, v85
	v_add_f32_e32 v170, v222, v170
	v_exp_f32_e32 v86, v86
	v_add_f32_e32 v170, v82, v170
	v_exp_f32_e32 v87, v87
	v_add_f32_e32 v170, v83, v170
	v_exp_f32_e32 v88, v88
	v_add_f32_e32 v170, v84, v170
	v_exp_f32_e32 v89, v89
	v_add_f32_e32 v170, v85, v170
	v_exp_f32_e32 v90, v90
	v_add_f32_e32 v170, v86, v170
	v_exp_f32_e32 v91, v91
	v_mfma_f32_32x32x64_f8f6f4 v[114:129], v[210:217], v[146:153], v[114:129]
	v_add_f32_e32 v170, v87, v170
	v_exp_f32_e32 v92, v92
	v_exp_f32_e32 v94, v94
	v_exp_f32_e32 v95, v95
	v_add_f32_e32 v170, v88, v170
	v_exp_f32_e32 v93, v93
	v_add_f32_e32 v170, v89, v170
	v_add_f32_e32 v170, v90, v170
	v_add_f32_e32 v170, v91, v170
	v_exp_f32_e32 v96, v96
	v_exp_f32_e32 v97, v97
	v_add_f32_e32 v170, v92, v170
	v_cvt_pk_fp8_f32 v130, v235, v236
	v_cvt_pk_fp8_f32 v134, v82, v83
	v_cvt_pk_fp8_f32 v131, v231, v232
	v_mfma_f32_32x32x64_f8f6f4 v[98:113], v[238:245], v[146:153], v[98:113]
	v_cvt_pk_fp8_f32 v135, v86, v87
	v_cvt_pk_fp8_f32 v132, v227, v228
	v_cvt_pk_fp8_f32 v136, v90, v91
	v_cvt_pk_fp8_f32 v133, v223, v224
	v_cvt_pk_fp8_f32 v137, v94, v95
	v_add_f32_e32 v170, v93, v170
	v_add_f32_e32 v170, v94, v170
	v_add_f32_e32 v170, v95, v170
	v_add_f32_e32 v170, v96, v170
	v_cvt_pk_fp8_f32 v130, v233, v234 op_sel:[0,0,1]
	v_cvt_pk_fp8_f32 v134, v84, v85 op_sel:[0,0,1]
	v_cvt_pk_fp8_f32 v131, v229, v230 op_sel:[0,0,1]
	v_cvt_pk_fp8_f32 v135, v88, v89 op_sel:[0,0,1]
	v_cvt_pk_fp8_f32 v132, v225, v226 op_sel:[0,0,1]
	v_cvt_pk_fp8_f32 v136, v92, v93 op_sel:[0,0,1]
	v_mfma_f32_32x32x64_f8f6f4 v[114:129], v[246:253], v[154:161], v[114:129]
	v_cvt_pk_fp8_f32 v133, v221, v222 op_sel:[0,0,1]
	v_cvt_pk_fp8_f32 v137, v96, v97 op_sel:[0,0,1]
	v_add_f32_e32 v170, v97, v170
	v_mov_b32_e32 v171, v170
	s_nop 1
	v_permlane32_swap_b32_e32 v170, v171
	v_mfma_f32_32x32x64_f8f6f4 v[98:113], v[178:185], v[154:161], v[98:113]
	ds_read_b128 v[86:89], v194
	ds_read_b128 v[82:85], v193
	ds_read_b128 v[90:93], v193 offset:2048
	ds_read_b128 v[94:97], v194 offset:2048
	s_nop 7
	v_max_f32_e32 v172, v114, v115
	v_max_f32_e32 v173, v114, v114
	s_waitcnt lgkmcnt(0)
	v_mfma_f32_32x32x64_f8f6f4 v[2:17], v[130:137], v[82:89], v[2:17]
	v_max3_f32 v172, v172, v116, v117
	v_max3_f32 v172, v172, v118, v119
	v_max3_f32 v172, v172, v120, v121
	v_max3_f32 v172, v172, v122, v123
	v_max3_f32 v172, v172, v124, v125
	v_max3_f32 v172, v172, v126, v127
	v_max3_f32 v172, v172, v128, v129
	v_max3_f32 v172, v172, v98, v99
	v_mfma_f32_32x32x64_f8f6f4 v[50:65], v[130:137], v[90:97], v[50:65]
	ds_read_b128 v[82:85], v193 offset:4096
	ds_read_b128 v[90:93], v193 offset:6144
	ds_read_b128 v[86:89], v194 offset:4096
	ds_read_b128 v[94:97], v194 offset:6144
	s_waitcnt lgkmcnt(0)
	v_mfma_f32_32x32x64_f8f6f4 v[34:49], v[130:137], v[82:89], v[34:49]
	v_max3_f32 v82, v172, v100, v101
	v_max3_f32 v82, v82, v102, v103
	v_max3_f32 v82, v82, v104, v105
	v_max3_f32 v82, v82, v106, v107
	v_max3_f32 v82, v82, v108, v109
	v_max3_f32 v82, v82, v110, v111
	v_max3_f32 v82, v82, v112, v113
	v_mov_b32_e32 v83, v82
	s_nop 1
	v_permlane32_swap_b32_e32 v82, v83
	v_max_f32_e32 v82, v82, v83
	v_cmp_ge_f32_e32 vcc, s85, v82
	s_cmp_eq_u64 vcc, exec
	v_mfma_f32_32x32x64_f8f6f4 v[18:33], v[130:137], v[90:97], v[18:33]
	v_mov_b32_e32 v172, 1.0
	s_cbranch_scc0 .LBB0_1086
	s_branch .LBB0_944

; template <bool FIRST>
; __device__ __forceinline__ void partialSM(f32x16& p0, f32x16& p1, float& m_reg, f32x16& nm16, float& alpha) {
;   float pmax = p0[0];
; #pragma unroll
;   for (int r = 1; r < 16; ++r) pmax = fmaxf(pmax, p0[r]);
; #pragma unroll
;   for (int r = 0; r < 16; ++r) pmax = fmaxf(pmax, p1[r]);
;   { auto rr = __builtin_amdgcn_permlane32_swap(__float_as_uint(pmax), __float_as_uint(pmax), false, false);
;     pmax = fmaxf(__uint_as_float(rr[0]), __uint_as_float(rr[1])); }
;   if (!FIRST && __builtin_expect(__all(pmax <= THR2), 1)) { alpha = 1.f; }
;   else { const float d = FIRST ? pmax : fmaxf(pmax, 0.f);
;     alpha = FIRST ? 1.f : __builtin_amdgcn_exp2f(-d); m_reg += d;
;     const float nm = -m_reg;
; #pragma unroll
;     for (int r = 0; r < 16; ++r) { p0[r] -= d; p1[r] -= d; float t = nm16[r]; asm volatile("v_mov_b32 %0, %1" : "+v"(t) : "v"(nm)); nm16[r] = t; } }
; #pragma unroll
;   for (int r = 0; r < 16; ++r) p0[r] = __builtin_amdgcn_exp2f(p0[r]);
; }
; __device__ __forceinline__ void finishSM(f32x16& p0, f32x16& p1, float alpha, float& l_reg, v8i& pa) {
; #pragma unroll
;   for (int r = 0; r < 16; ++r) p1[r] = __builtin_amdgcn_exp2f(p1[r]);
;   float ps = 0;
; #pragma unroll
;   for (int r = 0; r < 16; ++r) ps += p0[r];
; #pragma unroll
;   for (int r = 0; r < 16; ++r) ps += p1[r];
;   { auto rr = __builtin_amdgcn_permlane32_swap(__float_as_uint(ps), __float_as_uint(ps), false, false);
;     ps = __uint_as_float(rr[0]) + __uint_as_float(rr[1]); }
;   l_reg = l_reg * alpha + ps;
; #pragma unroll
;   for (int q = 0; q < 4; ++q) { int w0 = pa[q], w1 = pa[4 + q];
;     w0 = __builtin_amdgcn_cvt_pk_fp8_f32(p0[4 * q], p0[4 * q + 1], w0, false); w0 = __builtin_amdgcn_cvt_pk_fp8_f32(p0[4 * q + 2], p0[4 * q + 3], w0, true);
;     w1 = __builtin_amdgcn_cvt_pk_fp8_f32(p1[4 * q], p1[4 * q + 1], w1, false); w1 = __builtin_amdgcn_cvt_pk_fp8_f32(p1[4 * q + 2], p1[4 * q + 3], w1, true);
;     pa[q] = w0; pa[4 + q] = w1; }
; }
; __device__ __forceinline__ void qkt(f32x16& p0, f32x16& p1, const char* Ks, const v8i* qr, int r32, int hi, const f32x16& nm16) {
; #pragma unroll
;   for (int s = 0; s < 3; ++s) { const int c0 = 4 * s + 2 * hi;
;     const v8i a0 = __builtin_shufflevector(*reinterpret_cast<const v4i*>(Ks + k8_off(r32, c0)), *reinterpret_cast<const v4i*>(Ks + k8_off(r32, c0 + 1)), 0, 1, 2, 3, 4, 5, 6, 7);
.LBB0_946:
	s_mov_b32 m0, s86
	v_lshl_add_u64 v[82:83], v[168:169], 0, s[58:59]
	global_load_lds_dwordx4 v[82:83], off
	v_exp_f32_e32 v166, v114
	v_exp_f32_e32 v167, v115
	v_exp_f32_e32 v168, v116
	v_exp_f32_e32 v169, v117
	v_exp_f32_e32 v173, v118
	v_exp_f32_e32 v174, v119
	v_exp_f32_e32 v175, v120
	v_exp_f32_e32 v177, v121
	v_exp_f32_e32 v234, v122
	v_exp_f32_e32 v235, v123
	v_exp_f32_e32 v236, v124
	v_exp_f32_e32 v237, v125
	v_exp_f32_e32 v238, v126
	v_exp_f32_e32 v239, v127
	v_exp_f32_e32 v240, v128
	v_exp_f32_e32 v241, v129
	ds_read_b128 v[86:89], v197 offset:49152
	ds_read_b128 v[82:85], v196 offset:49152
	ds_read_b128 v[178:181], v196 offset:55296
	ds_read_b128 v[182:185], v197 offset:55296
	v_add_f32_e32 v164, 0, v166
	ds_read_b128 v[202:205], v198 offset:49152
	ds_read_b128 v[210:213], v198 offset:55296
	ds_read_b128 v[206:209], v199 offset:49152
	ds_read_b128 v[214:217], v199 offset:55296
	ds_read_b128 v[218:221], v200 offset:49152
	ds_read_b128 v[226:229], v200 offset:55296
	ds_read_b128 v[222:225], v201 offset:49152
	ds_read_b128 v[230:233], v201 offset:55296
	s_waitcnt lgkmcnt(0)
	v_mfma_f32_32x32x64_f8f6f4 v[114:129], v[82:89], v[138:145], v[66:81]
	v_add_f32_e32 v164, v167, v164
	v_add_f32_e32 v164, v168, v164
	v_add_f32_e32 v164, v169, v164
	v_add_f32_e32 v164, v173, v164
	v_add_f32_e32 v164, v174, v164
	v_add_f32_e32 v164, v175, v164
	v_add_f32_e32 v164, v177, v164
	v_add_f32_e32 v164, v234, v164
	v_add_f32_e32 v164, v235, v164
	v_add_f32_e32 v164, v236, v164
	v_add_f32_e32 v164, v237, v164
	v_exp_f32_e32 v98, v98
	v_add_f32_e32 v164, v238, v164
	v_exp_f32_e32 v99, v99
	v_add_f32_e32 v164, v239, v164
	v_mfma_f32_32x32x64_f8f6f4 v[82:97], v[178:185], v[138:145], v[66:81]
	v_exp_f32_e32 v100, v100
	v_add_f32_e32 v164, v240, v164
	v_exp_f32_e32 v101, v101
	v_add_f32_e32 v164, v241, v164
	v_exp_f32_e32 v102, v102
	v_add_f32_e32 v164, v98, v164
	v_exp_f32_e32 v103, v103
	v_add_f32_e32 v164, v99, v164
	v_exp_f32_e32 v104, v104
	v_add_f32_e32 v164, v100, v164
	v_exp_f32_e32 v105, v105
	v_add_f32_e32 v164, v101, v164
	v_exp_f32_e32 v106, v106
	v_add_f32_e32 v164, v102, v164
	v_exp_f32_e32 v107, v107
	v_mfma_f32_32x32x64_f8f6f4 v[114:129], v[202:209], v[146:153], v[114:129]
	v_add_f32_e32 v164, v103, v164
	v_exp_f32_e32 v108, v108
	v_exp_f32_e32 v110, v110
	v_exp_f32_e32 v111, v111
	v_add_f32_e32 v164, v104, v164
	v_exp_f32_e32 v109, v109
	v_add_f32_e32 v164, v105, v164
	v_add_f32_e32 v164, v106, v164
	v_add_f32_e32 v164, v107, v164
	v_exp_f32_e32 v112, v112
	v_exp_f32_e32 v113, v113
	v_add_f32_e32 v164, v108, v164
	v_cvt_pk_fp8_f32 v130, v166, v167
	v_cvt_pk_fp8_f32 v134, v98, v99
	v_cvt_pk_fp8_f32 v131, v173, v174
	v_mfma_f32_32x32x64_f8f6f4 v[82:97], v[210:217], v[146:153], v[82:97]
	v_cvt_pk_fp8_f32 v135, v102, v103
	v_cvt_pk_fp8_f32 v132, v234, v235
	v_cvt_pk_fp8_f32 v136, v106, v107
	v_cvt_pk_fp8_f32 v133, v238, v239
	v_cvt_pk_fp8_f32 v137, v110, v111
	v_add_f32_e32 v164, v109, v164
	v_add_f32_e32 v164, v110, v164
	v_add_f32_e32 v164, v111, v164
	v_add_f32_e32 v164, v112, v164
	v_cvt_pk_fp8_f32 v130, v168, v169 op_sel:[0,0,1]
	v_cvt_pk_fp8_f32 v134, v100, v101 op_sel:[0,0,1]
	v_cvt_pk_fp8_f32 v131, v175, v177 op_sel:[0,0,1]
	v_cvt_pk_fp8_f32 v135, v104, v105 op_sel:[0,0,1]
	v_cvt_pk_fp8_f32 v132, v236, v237 op_sel:[0,0,1]
	v_cvt_pk_fp8_f32 v136, v108, v109 op_sel:[0,0,1]
	v_mfma_f32_32x32x64_f8f6f4 v[114:129], v[218:225], v[154:161], v[114:129]
	v_cvt_pk_fp8_f32 v133, v240, v241 op_sel:[0,0,1]
	v_cvt_pk_fp8_f32 v137, v112, v113 op_sel:[0,0,1]
	v_add_f32_e32 v164, v113, v164
	v_mov_b32_e32 v165, v164
	s_nop 1
	v_permlane32_swap_b32_e32 v164, v165
	v_mfma_f32_32x32x64_f8f6f4 v[82:97], v[226:233], v[154:161], v[82:97]
	ds_read_b128 v[102:105], v194 offset:32768
	ds_read_b128 v[98:101], v193 offset:32768
	ds_read_b128 v[106:109], v193 offset:34816
	ds_read_b128 v[110:113], v194 offset:34816
	s_nop 7
	v_max_f32_e32 v166, v114, v115
	v_max_f32_e32 v167, v114, v114
	s_waitcnt lgkmcnt(0)
	v_mfma_f32_32x32x64_f8f6f4 v[2:17], v[130:137], v[98:105], v[2:17]
	v_max3_f32 v166, v166, v116, v117
	v_max3_f32 v166, v166, v118, v119
	v_max3_f32 v166, v166, v120, v121
	v_max3_f32 v166, v166, v122, v123
	v_max3_f32 v166, v166, v124, v125
	v_max3_f32 v166, v166, v126, v127
	v_max3_f32 v166, v166, v128, v129
	v_max3_f32 v166, v166, v82, v83
	v_mfma_f32_32x32x64_f8f6f4 v[50:65], v[130:137], v[106:113], v[50:65]
	ds_read_b128 v[98:101], v193 offset:36864
	ds_read_b128 v[106:109], v193 offset:38912
	ds_read_b128 v[102:105], v194 offset:36864
	ds_read_b128 v[110:113], v194 offset:38912
	s_waitcnt lgkmcnt(0)
	v_mfma_f32_32x32x64_f8f6f4 v[34:49], v[130:137], v[98:105], v[34:49]
	v_max3_f32 v98, v166, v84, v85
	v_max3_f32 v98, v98, v86, v87
	v_max3_f32 v98, v98, v88, v89
	v_max3_f32 v98, v98, v90, v91
	v_max3_f32 v98, v98, v92, v93
	v_max3_f32 v98, v98, v94, v95
	v_max3_f32 v98, v98, v96, v97
	v_mov_b32_e32 v99, v98
	s_nop 1
	v_permlane32_swap_b32_e32 v98, v99
	v_max_f32_e32 v98, v98, v99
	v_cmp_ge_f32_e32 vcc, s85, v98
	s_cmp_eq_u64 vcc, exec
	v_mfma_f32_32x32x64_f8f6f4 v[18:33], v[130:137], v[106:113], v[18:33]
	v_mov_b32_e32 v166, 1.0
	s_cbranch_scc0 .LBB0_1087
	s_branch .LBB0_951

; template <bool FIRST>
; __device__ __forceinline__ void partialSM(f32x16& p0, f32x16& p1, float& m_reg, f32x16& nm16, float& alpha) {
;   float pmax = p0[0];
; #pragma unroll
;   for (int r = 1; r < 16; ++r) pmax = fmaxf(pmax, p0[r]);
; #pragma unroll
;   for (int r = 0; r < 16; ++r) pmax = fmaxf(pmax, p1[r]);
;   { auto rr = __builtin_amdgcn_permlane32_swap(__float_as_uint(pmax), __float_as_uint(pmax), false, false);
;     pmax = fmaxf(__uint_as_float(rr[0]), __uint_as_float(rr[1])); }
;   if (!FIRST && __builtin_expect(__all(pmax <= THR2), 1)) { alpha = 1.f; }
;   else { const float d = FIRST ? pmax : fmaxf(pmax, 0.f);
;     alpha = FIRST ? 1.f : __builtin_amdgcn_exp2f(-d); m_reg += d;
;     const float nm = -m_reg;
; #pragma unroll
;     for (int r = 0; r < 16; ++r) { p0[r] -= d; p1[r] -= d; float t = nm16[r]; asm volatile("v_mov_b32 %0, %1" : "+v"(t) : "v"(nm)); nm16[r] = t; } }
; #pragma unroll
;   for (int r = 0; r < 16; ++r) p0[r] = __builtin_amdgcn_exp2f(p0[r]);
; }
; __device__ __forceinline__ void finishSM(f32x16& p0, f32x16& p1, float alpha, float& l_reg, v8i& pa) {
; #pragma unroll
;   for (int r = 0; r < 16; ++r) p1[r] = __builtin_amdgcn_exp2f(p1[r]);
;   float ps = 0;
; #pragma unroll
;   for (int r = 0; r < 16; ++r) ps += p0[r];
; #pragma unroll
;   for (int r = 0; r < 16; ++r) ps += p1[r];
;   { auto rr = __builtin_amdgcn_permlane32_swap(__float_as_uint(ps), __float_as_uint(ps), false, false);
;     ps = __uint_as_float(rr[0]) + __uint_as_float(rr[1]); }
;   l_reg = l_reg * alpha + ps;
; #pragma unroll
;   for (int q = 0; q < 4; ++q) { int w0 = pa[q], w1 = pa[4 + q];
;     w0 = __builtin_amdgcn_cvt_pk_fp8_f32(p0[4 * q], p0[4 * q + 1], w0, false); w0 = __builtin_amdgcn_cvt_pk_fp8_f32(p0[4 * q + 2], p0[4 * q + 3], w0, true);
;     w1 = __builtin_amdgcn_cvt_pk_fp8_f32(p1[4 * q], p1[4 * q + 1], w1, false); w1 = __builtin_amdgcn_cvt_pk_fp8_f32(p1[4 * q + 2], p1[4 * q + 3], w1, true);
;     pa[q] = w0; pa[4 + q] = w1; }
; }
; __device__ __forceinline__ void qkt(f32x16& p0, f32x16& p1, const char* Ks, const v8i* qr, int r32, int hi, const f32x16& nm16) {
; #pragma unroll
;   for (int s = 0; s < 3; ++s) { const int c0 = 4 * s + 2 * hi;
;     const v8i a0 = __builtin_shufflevector(*reinterpret_cast<const v4i*>(Ks + k8_off(r32, c0)), *reinterpret_cast<const v4i*>(Ks + k8_off(r32, c0 + 1)), 0, 1, 2, 3, 4, 5, 6, 7);
.LBB0_951:
	s_waitcnt vmcnt(0)
	s_barrier
	v_exp_f32_e32 v167, v114
	v_exp_f32_e32 v168, v115
	v_exp_f32_e32 v169, v116
	v_exp_f32_e32 v173, v117
	v_exp_f32_e32 v174, v118
	v_exp_f32_e32 v175, v119
	v_exp_f32_e32 v177, v120
	v_exp_f32_e32 v234, v121
	v_exp_f32_e32 v235, v122
	v_exp_f32_e32 v236, v123
	v_exp_f32_e32 v237, v124
	v_exp_f32_e32 v238, v125
	v_exp_f32_e32 v239, v126
	v_exp_f32_e32 v240, v127
	v_exp_f32_e32 v241, v128
	v_exp_f32_e32 v242, v129
	ds_read_b128 v[118:121], v197 offset:8192
	ds_read_b128 v[114:117], v196 offset:8192
	ds_read_b128 v[178:181], v196 offset:14336
	ds_read_b128 v[182:185], v197 offset:14336
	v_exp_f32_e32 v196, v82
	v_add_f32_e32 v82, 0, v167
	s_waitcnt lgkmcnt(0)
	v_mfma_f32_32x32x64_f8f6f4 v[98:113], v[114:121], v[138:145], v[66:81]
	ds_read_b128 v[202:205], v198 offset:8192
	ds_read_b128 v[210:213], v198 offset:14336
	ds_read_b128 v[206:209], v199 offset:8192
	ds_read_b128 v[214:217], v199 offset:14336
	ds_read_b128 v[218:221], v200 offset:8192
	ds_read_b128 v[226:229], v200 offset:14336
	ds_read_b128 v[222:225], v201 offset:8192
	ds_read_b128 v[230:233], v201 offset:14336
	v_add_f32_e32 v82, v168, v82
	v_add_f32_e32 v82, v169, v82
	v_add_f32_e32 v82, v173, v82
	v_add_f32_e32 v82, v174, v82
	v_add_f32_e32 v82, v175, v82
	v_add_f32_e32 v82, v177, v82
	v_add_f32_e32 v82, v234, v82
	v_add_f32_e32 v82, v235, v82
	v_add_f32_e32 v82, v236, v82
	v_add_f32_e32 v82, v237, v82
	v_add_f32_e32 v82, v238, v82
	v_add_f32_e32 v82, v239, v82
	v_exp_f32_e32 v197, v83
	v_add_f32_e32 v82, v240, v82
	v_mfma_f32_32x32x64_f8f6f4 v[114:129], v[178:185], v[138:145], v[66:81]
	v_exp_f32_e32 v84, v84
	v_add_f32_e32 v82, v241, v82
	v_exp_f32_e32 v85, v85
	v_add_f32_e32 v82, v242, v82
	v_exp_f32_e32 v86, v86
	v_add_f32_e32 v82, v196, v82
	v_exp_f32_e32 v87, v87
	v_add_f32_e32 v82, v197, v82
	v_exp_f32_e32 v88, v88
	v_add_f32_e32 v82, v84, v82
	v_exp_f32_e32 v89, v89
	v_add_f32_e32 v82, v85, v82
	v_exp_f32_e32 v90, v90
	v_add_f32_e32 v82, v86, v82
	v_exp_f32_e32 v91, v91
	s_waitcnt lgkmcnt(0)
	v_mfma_f32_32x32x64_f8f6f4 v[98:113], v[202:209], v[146:153], v[98:113]
	v_add_f32_e32 v82, v87, v82
	v_exp_f32_e32 v92, v92
	v_exp_f32_e32 v94, v94
	v_exp_f32_e32 v95, v95
	v_add_f32_e32 v82, v88, v82
	v_exp_f32_e32 v93, v93
	v_add_f32_e32 v82, v89, v82
	v_add_f32_e32 v82, v90, v82
	v_add_f32_e32 v82, v91, v82
	v_exp_f32_e32 v96, v96
	v_exp_f32_e32 v97, v97
	v_add_f32_e32 v82, v92, v82
	v_cvt_pk_fp8_f32 v130, v167, v168
	v_cvt_pk_fp8_f32 v134, v196, v197
	v_cvt_pk_fp8_f32 v131, v174, v175
	v_mfma_f32_32x32x64_f8f6f4 v[114:129], v[210:217], v[146:153], v[114:129]
	v_cvt_pk_fp8_f32 v135, v86, v87
	v_cvt_pk_fp8_f32 v132, v235, v236
	v_cvt_pk_fp8_f32 v136, v90, v91
	v_cvt_pk_fp8_f32 v133, v239, v240
	v_cvt_pk_fp8_f32 v137, v94, v95
	v_add_f32_e32 v82, v93, v82
	v_add_f32_e32 v82, v94, v82
	v_add_f32_e32 v82, v95, v82
	v_add_f32_e32 v82, v96, v82
	v_cvt_pk_fp8_f32 v130, v169, v173 op_sel:[0,0,1]
	v_cvt_pk_fp8_f32 v134, v84, v85 op_sel:[0,0,1]
	v_cvt_pk_fp8_f32 v131, v177, v234 op_sel:[0,0,1]
	v_cvt_pk_fp8_f32 v135, v88, v89 op_sel:[0,0,1]
	v_cvt_pk_fp8_f32 v132, v237, v238 op_sel:[0,0,1]
	v_cvt_pk_fp8_f32 v136, v92, v93 op_sel:[0,0,1]
	v_mfma_f32_32x32x64_f8f6f4 v[98:113], v[218:225], v[154:161], v[98:113]
	v_cvt_pk_fp8_f32 v133, v241, v242 op_sel:[0,0,1]
	v_cvt_pk_fp8_f32 v137, v96, v97 op_sel:[0,0,1]
	v_add_f32_e32 v82, v97, v82
	v_mov_b32_e32 v83, v82
	s_nop 1
	v_permlane32_swap_b32_e32 v82, v83
	v_mfma_f32_32x32x64_f8f6f4 v[114:129], v[226:233], v[154:161], v[114:129]
	ds_read_b128 v[88:91], v194 offset:40960
	ds_read_b128 v[84:87], v193 offset:40960
	ds_read_b128 v[138:141], v193 offset:43008
	ds_read_b128 v[142:145], v194 offset:43008
	s_nop 7
	v_max_f32_e32 v92, v98, v99
	v_max_f32_e32 v93, v98, v98
	s_waitcnt lgkmcnt(0)
	v_mfma_f32_32x32x64_f8f6f4 v[2:17], v[130:137], v[84:91], v[2:17]
	v_max3_f32 v92, v92, v100, v101
	v_max3_f32 v92, v92, v102, v103
	v_max3_f32 v92, v92, v104, v105
	v_max3_f32 v92, v92, v106, v107
	v_max3_f32 v92, v92, v108, v109
	v_max3_f32 v92, v92, v110, v111
	v_max3_f32 v92, v92, v112, v113
	v_max3_f32 v92, v92, v114, v115
	v_mfma_f32_32x32x64_f8f6f4 v[50:65], v[130:137], v[138:145], v[50:65]
	ds_read_b128 v[84:87], v193 offset:45056
	ds_read_b128 v[138:141], v193 offset:47104
	ds_read_b128 v[88:91], v194 offset:45056
	ds_read_b128 v[142:145], v194 offset:47104
	s_waitcnt lgkmcnt(0)
	v_mfma_f32_32x32x64_f8f6f4 v[34:49], v[130:137], v[84:91], v[34:49]
	v_max3_f32 v84, v92, v116, v117
	v_max3_f32 v84, v84, v118, v119
	v_max3_f32 v84, v84, v120, v121
	v_max3_f32 v84, v84, v122, v123
	v_max3_f32 v84, v84, v124, v125
	v_max3_f32 v84, v84, v126, v127
	v_max3_f32 v84, v84, v128, v129
	v_mov_b32_e32 v85, v84
	s_nop 1
	v_permlane32_swap_b32_e32 v84, v85
	v_max_f32_e32 v85, v84, v85
	v_cmp_ge_f32_e32 vcc, s85, v85
	s_cmp_eq_u64 vcc, exec
	v_mfma_f32_32x32x64_f8f6f4 v[18:33], v[130:137], v[138:145], v[18:33]
	v_mov_b32_e32 v84, 1.0
	s_cbranch_scc0 .LBB0_1088
	s_branch .LBB0_956

; __device__ __forceinline__ void attn_unit(const unsigned char* __restrict__ CQt, const unsigned char* __restrict__ Wh, const f32x2* __restrict__ cst, const unsigned char* __restrict__ Kh, const unsigned char* __restrict__ Vh, bf16* __restrict__ Ob, char* lds) {
;     ...
;       if (s3 == 2) {
; #pragma unroll
;         for (int r = 0; r < 16; r += 2) { const f32x2 c0 = cc[r >> 1], c1 = cc[8 + (r >> 1)];
;           const float x0 = a0[r], y0 = a0[r + 1], x1 = a1[r], y1 = a1[r + 1];
;           a0[r] = x0 * c0.x - y0 * c0.y; a0[r + 1] = y0 * c0.x + x0 * c0.y; a1[r] = x1 * c1.x - y1 * c1.y; a1[r + 1] = y1 * c1.x + x1 * c1.y; } }
; #pragma unroll
;       for (int q = 0; q < 4; ++q) { int u0 = 0, u1 = 0;
;         u0 = __builtin_amdgcn_cvt_pk_fp8_f32(a0[4 * q] * QS, a0[4 * q + 1] * QS, u0, false); u0 = __builtin_amdgcn_cvt_pk_fp8_f32(a0[4 * q + 2] * QS, a0[4 * q + 3] * QS, u0, true);
;         u1 = __builtin_amdgcn_cvt_pk_fp8_f32(a1[4 * q] * QS, a1[4 * q + 1] * QS, u1, false); u1 = __builtin_amdgcn_cvt_pk_fp8_f32(a1[4 * q + 2] * QS, a1[4 * q + 3] * QS, u1, true);
;         qr[s3][q] = u0; qr[s3][4 + q] = u1; }
.LBB0_2149:
	v_mul_f32_e32 v2, 0x3c553b94, v2
	v_mul_f32_e32 v3, 0x3c553b94, v3
	v_mov_b32_e32 v142, 0
	v_cvt_pk_fp8_f32 v142, v2, v3
	v_mul_f32_e32 v2, 0x3c553b94, v4
	v_mul_f32_e32 v3, 0x3c553b94, v5
	v_mov_b32_e32 v139, 0
	v_cvt_pk_fp8_f32 v142, v2, v3 op_sel:[0,0,1]
	v_mul_f32_e32 v2, 0x3c553b94, v22
	v_mul_f32_e32 v3, 0x3c553b94, v23
	v_cvt_pk_fp8_f32 v139, v2, v3
	v_mul_f32_e32 v4, 0x3c553b94, v6
	v_mul_f32_e32 v5, 0x3c553b94, v7
	v_mov_b32_e32 v143, 0
	v_cvt_pk_fp8_f32 v143, v4, v5
	v_mul_f32_e32 v2, 0x3c553b94, v24
	v_mul_f32_e32 v3, 0x3c553b94, v25
	v_cvt_pk_fp8_f32 v139, v2, v3 op_sel:[0,0,1]
	v_mul_f32_e32 v2, 0x3c553b94, v8
	v_mul_f32_e32 v3, 0x3c553b94, v9
	v_cvt_pk_fp8_f32 v143, v2, v3 op_sel:[0,0,1]
	v_mul_f32_e32 v2, 0x3c553b94, v26
	v_mul_f32_e32 v3, 0x3c553b94, v27
	v_mov_b32_e32 v140, 0
	v_cvt_pk_fp8_f32 v140, v2, v3
	v_mul_f32_e32 v4, 0x3c553b94, v10
	v_mul_f32_e32 v5, 0x3c553b94, v11
	v_mov_b32_e32 v144, 0
	v_cvt_pk_fp8_f32 v144, v4, v5
	v_mul_f32_e32 v2, 0x3c553b94, v28
	v_mul_f32_e32 v3, 0x3c553b94, v29
	v_cvt_pk_fp8_f32 v140, v2, v3 op_sel:[0,0,1]
	v_mul_f32_e32 v2, 0x3c553b94, v12
	v_mul_f32_e32 v3, 0x3c553b94, v13
	v_cvt_pk_fp8_f32 v144, v2, v3 op_sel:[0,0,1]
	v_mul_f32_e32 v2, 0x3c553b94, v30
	v_mul_f32_e32 v3, 0x3c553b94, v31
	v_mov_b32_e32 v141, 0
	v_cvt_pk_fp8_f32 v141, v2, v3
	v_mul_f32_e32 v4, 0x3c553b94, v14
	v_mul_f32_e32 v5, 0x3c553b94, v15
	v_mov_b32_e32 v145, 0
	v_cvt_pk_fp8_f32 v145, v4, v5
	v_mul_f32_e32 v2, 0x3c553b94, v32
	v_mul_f32_e32 v3, 0x3c553b94, v33
	v_cvt_pk_fp8_f32 v141, v2, v3 op_sel:[0,0,1]
	v_mul_f32_e32 v2, 0x3c553b94, v16
	v_mul_f32_e32 v3, 0x3c553b94, v17
	v_cvt_pk_fp8_f32 v145, v2, v3 op_sel:[0,0,1]
	v_mul_f32_e32 v2, 0x3c553b94, v50
	v_mul_f32_e32 v3, 0x3c553b94, v51
	v_mov_b32_e32 v146, 0
	v_cvt_pk_fp8_f32 v146, v2, v3
	v_mul_f32_e32 v4, 0x3c553b94, v34
	v_mul_f32_e32 v5, 0x3c553b94, v35
	v_mov_b32_e32 v150, 0
	v_cvt_pk_fp8_f32 v150, v4, v5
	v_mul_f32_e32 v2, 0x3c553b94, v52
	v_mul_f32_e32 v3, 0x3c553b94, v53
	v_cvt_pk_fp8_f32 v146, v2, v3 op_sel:[0,0,1]
	v_mul_f32_e32 v2, 0x3c553b94, v36
	v_mul_f32_e32 v3, 0x3c553b94, v37
	v_cvt_pk_fp8_f32 v150, v2, v3 op_sel:[0,0,1]
	v_mul_f32_e32 v2, 0x3c553b94, v54
	v_mul_f32_e32 v3, 0x3c553b94, v55
	v_mov_b32_e32 v147, 0
	v_cvt_pk_fp8_f32 v147, v2, v3
	v_mul_f32_e32 v4, 0x3c553b94, v38
	v_mul_f32_e32 v5, 0x3c553b94, v39
	v_mov_b32_e32 v151, 0
	v_cvt_pk_fp8_f32 v151, v4, v5
	v_mul_f32_e32 v2, 0x3c553b94, v56
	v_mul_f32_e32 v3, 0x3c553b94, v57
	v_cvt_pk_fp8_f32 v147, v2, v3 op_sel:[0,0,1]
	v_mul_f32_e32 v2, 0x3c553b94, v40
	v_mul_f32_e32 v3, 0x3c553b94, v41
	v_cvt_pk_fp8_f32 v151, v2, v3 op_sel:[0,0,1]
	v_mul_f32_e32 v2, 0x3c553b94, v58
	v_mul_f32_e32 v3, 0x3c553b94, v59
	v_mov_b32_e32 v148, 0
	v_cvt_pk_fp8_f32 v148, v2, v3
	v_mul_f32_e32 v4, 0x3c553b94, v42
	v_mul_f32_e32 v5, 0x3c553b94, v43
	v_mov_b32_e32 v152, 0
	v_cvt_pk_fp8_f32 v152, v4, v5
	v_mul_f32_e32 v2, 0x3c553b94, v60
	v_mul_f32_e32 v3, 0x3c553b94, v61
	v_cvt_pk_fp8_f32 v148, v2, v3 op_sel:[0,0,1]
	v_mul_f32_e32 v2, 0x3c553b94, v44
	v_mul_f32_e32 v3, 0x3c553b94, v45
	v_cvt_pk_fp8_f32 v152, v2, v3 op_sel:[0,0,1]
	v_mul_f32_e32 v2, 0x3c553b94, v62
	v_mul_f32_e32 v3, 0x3c553b94, v63
	v_mov_b32_e32 v149, 0
	v_cvt_pk_fp8_f32 v149, v2, v3
	v_mul_f32_e32 v4, 0x3c553b94, v46
	v_mul_f32_e32 v5, 0x3c553b94, v47
	v_mov_b32_e32 v153, 0
	v_cvt_pk_fp8_f32 v153, v4, v5
	v_mul_f32_e32 v2, 0x3c553b94, v64
	v_mul_f32_e32 v3, 0x3c553b94, v65
	v_cvt_pk_fp8_f32 v149, v2, v3 op_sel:[0,0,1]
	v_mul_f32_e32 v2, 0x3c553b94, v48
	v_mul_f32_e32 v3, 0x3c553b94, v49
	v_cvt_pk_fp8_f32 v153, v2, v3 op_sel:[0,0,1]
	s_waitcnt vmcnt(0)
	v_pk_mul_f32 v[2:3], v[134:135], v[82:83]
	v_mov_b32_e32 v154, 0
	v_sub_f32_e32 v4, v2, v3
	v_pk_mul_f32 v[2:3], v[134:135], v[82:83] op_sel:[0,1] op_sel_hi:[1,0]
	v_mov_b32_e32 v158, 0
	v_add_f32_e32 v5, v2, v3
	v_pk_mul_f32 v[2:3], v[136:137], v[84:85]
	s_mov_b32 m0, s88
	v_sub_f32_e32 v10, v2, v3
	v_pk_mul_f32 v[2:3], v[136:137], v[84:85] op_sel:[0,1] op_sel_hi:[1,0]
	v_or_b32_e32 v99, 1, v156
	v_add_f32_e32 v11, v2, v3
	v_pk_mul_f32 v[2:3], v[130:131], v[86:87]
	v_lshrrev_b32_e32 v65, 2, v189
	v_sub_f32_e32 v34, v2, v3
	v_pk_mul_f32 v[2:3], v[130:131], v[86:87] op_sel:[0,1] op_sel_hi:[1,0]
	v_mul_u32_u24_e32 v64, 0xc0, v170
	v_add_f32_e32 v35, v2, v3
	v_pk_mul_f32 v[2:3], v[132:133], v[88:89]
	v_mul_f32_e32 v18, 0x3c553b94, v18
	v_sub_f32_e32 v36, v2, v3
	v_pk_mul_f32 v[2:3], v[132:133], v[88:89] op_sel:[0,1] op_sel_hi:[1,0]
	v_mul_f32_e32 v19, 0x3c553b94, v19
	v_add_f32_e32 v37, v2, v3
	v_pk_mul_f32 v[2:3], v[126:127], v[90:91]
	v_mov_b32_e32 v138, 0
	v_sub_f32_e32 v50, v2, v3
	v_pk_mul_f32 v[2:3], v[126:127], v[90:91] op_sel:[0,1] op_sel_hi:[1,0]
	v_cvt_pk_fp8_f32 v138, v18, v19
	v_add_f32_e32 v51, v2, v3
	v_pk_mul_f32 v[2:3], v[128:129], v[92:93]
	v_mul_f32_e32 v18, 0x3c553b94, v20
	v_sub_f32_e32 v52, v2, v3
	v_pk_mul_f32 v[2:3], v[128:129], v[92:93] op_sel:[0,1] op_sel_hi:[1,0]
	v_mul_f32_e32 v19, 0x3c553b94, v21
	v_add_f32_e32 v53, v2, v3
	v_pk_mul_f32 v[2:3], v[122:123], v[94:95]
	v_cvt_pk_fp8_f32 v138, v18, v19 op_sel:[0,0,1]
	v_sub_f32_e32 v54, v2, v3
	v_pk_mul_f32 v[2:3], v[122:123], v[94:95] op_sel:[0,1] op_sel_hi:[1,0]
	v_mov_b32_e32 v155, 0
	v_add_f32_e32 v55, v2, v3
	v_pk_mul_f32 v[2:3], v[124:125], v[96:97]
	v_mov_b32_e32 v159, 0
	v_sub_f32_e32 v56, v2, v3
	v_pk_mul_f32 v[2:3], v[124:125], v[96:97] op_sel:[0,1] op_sel_hi:[1,0]
	v_or_b32_e32 v100, 4, v156
	v_add_f32_e32 v57, v2, v3
	v_pk_mul_f32 v[2:3], v[118:119], v[66:67]
	v_or_b32_e32 v101, 5, v156
	v_sub_f32_e32 v6, v2, v3
	v_pk_mul_f32 v[2:3], v[118:119], v[66:67] op_sel:[0,1] op_sel_hi:[1,0]
; __device__ __forceinline__ void qkt(f32x16& p0, f32x16& p1, const char* Ks, const v8i* qr, int r32, int hi, const f32x16& nm16) {
; #pragma unroll
;   for (int s = 0; s < 3; ++s) { const int c0 = 4 * s + 2 * hi;
;     const v8i a0 = __builtin_shufflevector(*reinterpret_cast<const v4i*>(Ks + k8_off(r32, c0)), *reinterpret_cast<const v4i*>(Ks + k8_off(r32, c0 + 1)), 0, 1, 2, 3, 4, 5, 6, 7);
;     const v8i a1 = __builtin_shufflevector(*reinterpret_cast<const v4i*>(Ks + 32 * DQK + k8_off(r32, c0)), *reinterpret_cast<const v4i*>(Ks + 32 * DQK + k8_off(r32, c0 + 1)), 0, 1, 2, 3, 4, 5, 6, 7);
;     p0 = __builtin_amdgcn_mfma_scale_f32_32x32x64_f8f6f4(a0, qr[s], s == 0 ? nm16 : p0, 0, 0, 0, 0, 0, 0);
;     p1 = __builtin_amdgcn_mfma_scale_f32_32x32x64_f8f6f4(a1, qr[s], s == 0 ? nm16 : p1, 0, 0, 0, 0, 0, 0); }
; }
; __device__ __forceinline__ void attn_unit(const unsigned char* __restrict__ CQt, const unsigned char* __restrict__ Wh, const f32x2* __restrict__ cst, const unsigned char* __restrict__ Kh, const unsigned char* __restrict__ Vh, bf16* __restrict__ Ob, char* lds) {
;     ...
;       if (s3 == 2) {
; #pragma unroll
;         for (int r = 0; r < 16; r += 2) { const f32x2 c0 = cc[r >> 1], c1 = cc[8 + (r >> 1)];
;           const float x0 = a0[r], y0 = a0[r + 1], x1 = a1[r], y1 = a1[r + 1];
;           a0[r] = x0 * c0.x - y0 * c0.y; a0[r + 1] = y0 * c0.x + x0 * c0.y; a1[r] = x1 * c1.x - y1 * c1.y; a1[r + 1] = y1 * c1.x + x1 * c1.y; } }
; #pragma unroll
;       for (int q = 0; q < 4; ++q) { int u0 = 0, u1 = 0;
;         u0 = __builtin_amdgcn_cvt_pk_fp8_f32(a0[4 * q] * QS, a0[4 * q + 1] * QS, u0, false); u0 = __builtin_amdgcn_cvt_pk_fp8_f32(a0[4 * q + 2] * QS, a0[4 * q + 3] * QS, u0, true);
;         u1 = __builtin_amdgcn_cvt_pk_fp8_f32(a1[4 * q] * QS, a1[4 * q + 1] * QS, u1, false); u1 = __builtin_amdgcn_cvt_pk_fp8_f32(a1[4 * q + 2] * QS, a1[4 * q + 3] * QS, u1, true);
;         qr[s3][q] = u0; qr[s3][4 + q] = u1; }
;     }
;     asm volatile("s_waitcnt lgkmcnt(0)" ::: "memory"); __builtin_amdgcn_s_barrier(); asm volatile("" ::: "memory");
;   }
;   ADMA(1, 1);
;   qkt(pA0, pA1, lds + KS(0), qr, r32, hi, nm16); partialSM<true>(pA0, pA1, m_reg, nm16, alA);
	v_mul_f32_e32 v6, 0x3c553b94, v6
	v_add_f32_e32 v7, v2, v3
	v_pk_mul_f32 v[2:3], v[120:121], v[68:69]
	v_mul_f32_e32 v7, 0x3c553b94, v7
	v_sub_f32_e32 v8, v2, v3
	v_pk_mul_f32 v[2:3], v[120:121], v[68:69] op_sel:[0,1] op_sel_hi:[1,0]
	v_cvt_pk_fp8_f32 v154, v6, v7
	v_add_f32_e32 v9, v2, v3
	v_pk_mul_f32 v[2:3], v[114:115], v[70:71]
	v_bitop3_b32 v6, v99, v65, 3 bitop3:0x78
	v_sub_f32_e32 v12, v2, v3
	v_pk_mul_f32 v[2:3], v[114:115], v[70:71] op_sel:[0,1] op_sel_hi:[1,0]
	v_lshlrev_b32_e32 v203, 4, v6
	v_add_f32_e32 v13, v2, v3
	v_pk_mul_f32 v[2:3], v[116:117], v[72:73]
	v_or_b32_e32 v6, v203, v64
	v_sub_f32_e32 v38, v2, v3
	v_pk_mul_f32 v[2:3], v[116:117], v[72:73] op_sel:[0,1] op_sel_hi:[1,0]
	v_add_u32_e32 v197, 0, v6
	v_add_f32_e32 v39, v2, v3
	v_pk_mul_f32 v[2:3], v[110:111], v[74:75]
	v_mul_f32_e32 v42, 0x3c553b94, v12
	v_sub_f32_e32 v40, v2, v3
	v_pk_mul_f32 v[2:3], v[110:111], v[74:75] op_sel:[0,1] op_sel_hi:[1,0]
	v_mul_f32_e32 v43, 0x3c553b94, v13
	v_add_f32_e32 v41, v2, v3
	v_pk_mul_f32 v[2:3], v[112:113], v[76:77]
	v_cvt_pk_fp8_f32 v155, v42, v43
	v_sub_f32_e32 v58, v2, v3
	v_pk_mul_f32 v[2:3], v[112:113], v[76:77] op_sel:[0,1] op_sel_hi:[1,0]
	v_or_b32_e32 v102, 8, v156
	v_add_f32_e32 v59, v2, v3
	v_pk_mul_f32 v[2:3], v[106:107], v[78:79]
	v_or_b32_e32 v103, 9, v156
	v_sub_f32_e32 v60, v2, v3
	v_pk_mul_f32 v[2:3], v[106:107], v[78:79] op_sel:[0,1] op_sel_hi:[1,0]
	v_mul_f32_e32 v10, 0x3c553b94, v10
	v_add_f32_e32 v61, v2, v3
	v_pk_mul_f32 v[2:3], v[108:109], v[80:81]
	v_mul_f32_e32 v11, 0x3c553b94, v11
	v_sub_f32_e32 v62, v2, v3
	v_pk_mul_f32 v[2:3], v[108:109], v[80:81] op_sel:[0,1] op_sel_hi:[1,0]
	v_mul_f32_e32 v50, 0x3c553b94, v50
	v_add_f32_e32 v63, v2, v3
	v_mul_f32_e32 v2, 0x3c553b94, v8
	v_mul_f32_e32 v3, 0x3c553b94, v9
	v_cvt_pk_fp8_f32 v154, v2, v3 op_sel:[0,0,1]
	v_mul_f32_e32 v2, 0x3c553b94, v4
	v_mul_f32_e32 v3, 0x3c553b94, v5
	v_cvt_pk_fp8_f32 v158, v2, v3
	v_lshl_add_u64 v[2:3], v[168:169], 0, 64
	global_load_lds_dwordx4 v[2:3], off
	v_bitop3_b32 v2, v156, v65, 3 bitop3:0x78
	v_lshlrev_b32_e32 v202, 4, v2
	v_or_b32_e32 v2, v202, v64
	v_add_u32_e32 v196, 0, v2
	ds_read_b128 v[2:5], v196 offset:8192
	ds_read_b128 v[6:9], v197 offset:8192
	s_waitcnt lgkmcnt(0)
	v_mfma_f32_32x32x64_f8f6f4 v[18:33], v[2:9], v[138:145], 0
	v_mul_f32_e32 v4, 0x3c553b94, v34
	v_mul_f32_e32 v5, 0x3c553b94, v35
	v_cvt_pk_fp8_f32 v159, v4, v5
	v_mul_f32_e32 v2, 0x3c553b94, v38
	v_mul_f32_e32 v3, 0x3c553b94, v39
	v_cvt_pk_fp8_f32 v155, v2, v3 op_sel:[0,0,1]
	v_mul_f32_e32 v2, 0x3c553b94, v36
	v_mul_f32_e32 v3, 0x3c553b94, v37
	v_cvt_pk_fp8_f32 v159, v2, v3 op_sel:[0,0,1]
	v_mul_f32_e32 v2, 0x3c553b94, v40
	v_mul_f32_e32 v3, 0x3c553b94, v41
	v_mov_b32_e32 v156, 0
	v_cvt_pk_fp8_f32 v156, v2, v3
	v_bitop3_b32 v2, v100, v65, 3 bitop3:0x78
	v_bitop3_b32 v6, v101, v65, 3 bitop3:0x78
	v_lshl_add_u32 v2, v2, 4, v64
	v_lshl_add_u32 v6, v6, 4, v64
	v_cvt_pk_fp8_f32 v158, v10, v11 op_sel:[0,0,1]
	ds_read_b128 v[10:13], v196 offset:14336
	ds_read_b128 v[14:17], v197 offset:14336
	v_add_u32_e32 v198, 0, v2
	v_add_u32_e32 v199, 0, v6
	ds_read_b128 v[2:5], v198 offset:8192
	ds_read_b128 v[6:9], v199 offset:8192
	s_waitcnt lgkmcnt(0)
	v_mfma_f32_32x32x64_f8f6f4 v[34:49], v[10:17], v[138:145], 0
	v_mul_f32_e32 v51, 0x3c553b94, v51
	v_mov_b32_e32 v160, 0
	v_cvt_pk_fp8_f32 v160, v50, v51
	v_mov_b32_e32 v157, 0
	v_mul_f32_e32 v10, 0x3c553b94, v58
	v_mul_f32_e32 v11, 0x3c553b94, v59
	v_mov_b32_e32 v161, 0
	v_cvt_pk_fp8_f32 v156, v10, v11 op_sel:[0,0,1]
	ds_read_b128 v[10:13], v198 offset:14336
	ds_read_b128 v[14:17], v199 offset:14336
	s_mov_b32 s8, s9
	s_mov_b32 s10, s9
	s_mov_b32 s11, s9
	s_mov_b32 s12, s9
	s_mov_b32 s13, s9
	s_mov_b32 s14, s9
	v_mfma_f32_32x32x64_f8f6f4 v[18:33], v[2:9], v[146:153], v[18:33]
	v_mul_f32_e32 v4, 0x3c553b94, v60
	v_mul_f32_e32 v5, 0x3c553b94, v61
	v_cvt_pk_fp8_f32 v157, v4, v5
	v_mul_f32_e32 v2, 0x3c553b94, v52
	v_mul_f32_e32 v3, 0x3c553b94, v53
	v_cvt_pk_fp8_f32 v160, v2, v3 op_sel:[0,0,1]
	v_mul_f32_e32 v2, 0x3c553b94, v62
	v_mul_f32_e32 v3, 0x3c553b94, v63
	v_cvt_pk_fp8_f32 v157, v2, v3 op_sel:[0,0,1]
	v_mul_f32_e32 v2, 0x3c553b94, v54
	v_mul_f32_e32 v3, 0x3c553b94, v55
	v_cvt_pk_fp8_f32 v161, v2, v3
	v_bitop3_b32 v2, v102, v65, 3 bitop3:0x78
	v_bitop3_b32 v6, v103, v65, 3 bitop3:0x78
	v_lshl_add_u32 v2, v2, 4, v64
	v_lshl_add_u32 v6, v6, 4, v64
	v_add_u32_e32 v200, 0, v2
	v_add_u32_e32 v201, 0, v6
	ds_read_b128 v[2:5], v200 offset:8192
	ds_read_b128 v[6:9], v201 offset:8192
	s_waitcnt lgkmcnt(0)
; #define AWAIT(n) asm volatile("s_waitcnt vmcnt(" #n ")" ::: "memory")
; #define ABAR() do { asm volatile("" ::: "memory"); __builtin_amdgcn_s_barrier(); asm volatile("" ::: "memory"); } while (0)
; template <bool FIRST>
; __device__ __forceinline__ void partialSM(f32x16& p0, f32x16& p1, float& m_reg, f32x16& nm16, float& alpha) {
;   float pmax = p0[0];
; #pragma unroll
;   for (int r = 1; r < 16; ++r) pmax = fmaxf(pmax, p0[r]);
; #pragma unroll
;   for (int r = 0; r < 16; ++r) pmax = fmaxf(pmax, p1[r]);
;   { auto rr = __builtin_amdgcn_permlane32_swap(__float_as_uint(pmax), __float_as_uint(pmax), false, false);
;     pmax = fmaxf(__uint_as_float(rr[0]), __uint_as_float(rr[1])); }
;   if (!FIRST && __builtin_expect(__all(pmax <= THR2), 1)) { alpha = 1.f; }
;   else { const float d = FIRST ? pmax : fmaxf(pmax, 0.f);
;     alpha = FIRST ? 1.f : __builtin_amdgcn_exp2f(-d); m_reg += d;
;     const float nm = -m_reg;
; #pragma unroll
;     for (int r = 0; r < 16; ++r) { p0[r] -= d; p1[r] -= d; float t = nm16[r]; asm volatile("v_mov_b32 %0, %1" : "+v"(t) : "v"(nm)); nm16[r] = t; } }
; #pragma unroll
;   for (int r = 0; r < 16; ++r) p0[r] = __builtin_amdgcn_exp2f(p0[r]);
; __device__ __forceinline__ void attn_unit(const unsigned char* __restrict__ CQt, const unsigned char* __restrict__ Wh, const f32x2* __restrict__ cst, const unsigned char* __restrict__ Kh, const unsigned char* __restrict__ Vh, bf16* __restrict__ Ob, char* lds) {
;     ...
; #pragma unroll
;       for (int q = 0; q < 4; ++q) { int u0 = 0, u1 = 0;
;         u0 = __builtin_amdgcn_cvt_pk_fp8_f32(a0[4 * q] * QS, a0[4 * q + 1] * QS, u0, false); u0 = __builtin_amdgcn_cvt_pk_fp8_f32(a0[4 * q + 2] * QS, a0[4 * q + 3] * QS, u0, true);
;         u1 = __builtin_amdgcn_cvt_pk_fp8_f32(a1[4 * q] * QS, a1[4 * q + 1] * QS, u1, false); u1 = __builtin_amdgcn_cvt_pk_fp8_f32(a1[4 * q + 2] * QS, a1[4 * q + 3] * QS, u1, true);
;         qr[s3][q] = u0; qr[s3][4 + q] = u1; }
;     }
;     asm volatile("s_waitcnt lgkmcnt(0)" ::: "memory"); __builtin_amdgcn_s_barrier(); asm volatile("" ::: "memory");
;   }
;   ADMA(1, 1);
;   qkt(pA0, pA1, lds + KS(0), qr, r32, hi, nm16); partialSM<true>(pA0, pA1, m_reg, nm16, alA);
;   AWAIT(0); ABAR();
	v_mfma_f32_32x32x64_f8f6f4 v[34:49], v[10:17], v[146:153], v[34:49]
	v_mul_f32_e32 v10, 0x3c553b94, v56
	v_mul_f32_e32 v11, 0x3c553b94, v57
	v_cvt_pk_fp8_f32 v161, v10, v11 op_sel:[0,0,1]
	ds_read_b128 v[50:53], v200 offset:14336
	ds_read_b128 v[54:57], v201 offset:14336
	s_mov_b32 s15, s9
	s_mov_b32 s16, s9
	s_mov_b32 s17, s9
	s_mov_b32 s18, s9
	s_mov_b32 s19, s9
	s_mov_b32 s20, s9
	s_mov_b32 s21, s9
	s_mov_b32 s22, s9
	s_mov_b32 s23, s9
	v_mov_b32_e32 v66, 0
	v_mov_b32_e32 v67, 0
	v_mfma_f32_32x32x64_f8f6f4 v[18:33], v[2:9], v[154:161], v[18:33]
	v_mov_b64_e32 v[2:3], s[8:9]
	v_mov_b64_e32 v[4:5], s[10:11]
	v_mov_b64_e32 v[6:7], s[12:13]
	v_mov_b64_e32 v[8:9], s[14:15]
	v_mov_b64_e32 v[10:11], s[16:17]
	v_mov_b64_e32 v[12:13], s[18:19]
	v_mov_b64_e32 v[14:15], s[20:21]
	v_mov_b64_e32 v[16:17], s[22:23]
	s_lshl_b32 s8, s33, 10
	s_and_b32 s8, s8, 0xffff0000
	v_mov_b32_e32 v68, 0
	v_mov_b32_e32 v69, 0
	v_mov_b32_e32 v70, 0
	v_mov_b32_e32 v71, 0
	v_mov_b32_e32 v72, 0
	s_waitcnt lgkmcnt(0)
	v_mfma_f32_32x32x64_f8f6f4 v[34:49], v[50:57], v[154:161], v[34:49]
	s_nop 2
	v_max_f32_e32 v50, v18, v19
	v_max3_f32 v50, v50, v20, v21
	v_max3_f32 v50, v50, v22, v23
	v_max3_f32 v50, v50, v24, v25
	v_max3_f32 v50, v50, v26, v27
	v_max3_f32 v50, v50, v28, v29
	v_max3_f32 v50, v50, v30, v31
	v_max3_f32 v50, v50, v32, v33
	v_mov_b32_e32 v73, 0
	v_mov_b32_e32 v74, 0
	v_mov_b32_e32 v75, 0
	v_mov_b32_e32 v76, 0
	v_mov_b32_e32 v77, 0
	s_nop 1
	v_max3_f32 v50, v50, v34, v35
	v_max3_f32 v50, v50, v36, v37
	v_max3_f32 v50, v50, v38, v39
	v_max3_f32 v50, v50, v40, v41
	v_max3_f32 v50, v50, v42, v43
	v_max3_f32 v50, v50, v44, v45
	v_max3_f32 v50, v50, v46, v47
	v_max3_f32 v50, v50, v48, v49
	v_mov_b32_e32 v51, v50
	s_nop 1
	v_permlane32_swap_b32_e32 v50, v51
	v_max_f32_e32 v50, v50, v51
	v_sub_f32_e32 v18, v18, v50
	v_add_f32_e32 v195, 0, v50
	v_sub_f32_e32 v19, v19, v50
	v_sub_f32_e32 v20, v20, v50
	v_sub_f32_e32 v21, v21, v50
	v_sub_f32_e32 v22, v22, v50
	v_sub_f32_e32 v23, v23, v50
	v_sub_f32_e32 v24, v24, v50
	v_sub_f32_e32 v25, v25, v50
	v_sub_f32_e32 v26, v26, v50
	v_sub_f32_e32 v27, v27, v50
	v_sub_f32_e32 v28, v28, v50
	v_sub_f32_e32 v29, v29, v50
	v_sub_f32_e32 v30, v30, v50
	v_mov_b32_e32 v78, 0
	v_sub_f32_e32 v31, v31, v50
	v_mov_b32_e32 v79, 0
	v_sub_f32_e32 v32, v32, v50
	v_mov_b32_e32 v80, 0
	v_sub_f32_e32 v33, v33, v50
	v_mov_b32_e32 v81, 0
	v_exp_f32_e32 v235, v18
	v_lshl_or_b32 v18, v171, 10, s8
	s_lshl_b32 s2, s2, 2
	v_xor_b32_e32 v51, 0x80000000, v195
	v_mov_b32 v66, v51
	v_mov_b32 v67, v51
	v_mov_b32 v68, v51
	v_mov_b32 v69, v51
	v_mov_b32 v70, v51
	v_mov_b32 v71, v51
	v_mov_b32 v72, v51
	v_mov_b32 v73, v51
	v_mov_b32 v74, v51
	v_mov_b32 v75, v51
	v_mov_b32 v76, v51
	v_mov_b32 v77, v51
	v_mov_b32 v78, v51
	v_mov_b32 v79, v51
	v_mov_b32 v80, v51
	v_mov_b32 v81, v51
	v_exp_f32_e32 v236, v19
	v_exp_f32_e32 v233, v20
	v_exp_f32_e32 v234, v21
	v_exp_f32_e32 v231, v22
	v_exp_f32_e32 v232, v23
	v_exp_f32_e32 v229, v24
	v_exp_f32_e32 v230, v25
	v_exp_f32_e32 v227, v26
	v_exp_f32_e32 v228, v27
	v_exp_f32_e32 v225, v28
	v_exp_f32_e32 v226, v29
	v_exp_f32_e32 v223, v30
	v_exp_f32_e32 v224, v31
	v_exp_f32_e32 v221, v32
	v_exp_f32_e32 v222, v33
	s_waitcnt vmcnt(0)
	v_and_or_b32 v18, v18, s84, v172
	s_add_i32 s93, s2, 0
	s_barrier
	v_ashrrev_i32_e32 v19, 31, v18
	v_lshlrev_b32_e32 v98, 4, v190
	v_mov_b32_e32 v162, 0
	v_sub_f32_e32 v97, v49, v50
	v_sub_f32_e32 v96, v48, v50
	v_sub_f32_e32 v95, v47, v50
	v_sub_f32_e32 v94, v46, v50
	v_sub_f32_e32 v93, v45, v50
	v_sub_f32_e32 v92, v44, v50
	v_sub_f32_e32 v91, v43, v50
	v_sub_f32_e32 v90, v42, v50
	v_sub_f32_e32 v89, v41, v50
	v_sub_f32_e32 v88, v40, v50
	v_sub_f32_e32 v87, v39, v50
	v_sub_f32_e32 v86, v38, v50
	v_sub_f32_e32 v85, v37, v50
	v_sub_f32_e32 v84, v36, v50
	v_sub_f32_e32 v83, v35, v50
	v_sub_f32_e32 v82, v34, v50
	v_lshl_add_u32 v204, v170, 6, 0
	v_cmp_gt_u32_e64 s[2:3], 32, v171
	v_lshl_add_u32 v192, v170, 2, s93
	v_lshl_add_u64 v[170:171], s[66:67], 0, v[18:19]
	v_mov_b64_e32 v[64:65], v[16:17]
	v_mov_b64_e32 v[48:49], v[16:17]
	v_mov_b64_e32 v[32:33], v[16:17]
	v_add_u32_e32 v191, s93, v98
	v_lshl_add_u64 v[172:173], v[166:167], 0, s[4:5]
	v_lshl_add_u64 v[174:175], s[4:5], 0, v[164:165]
	s_add_u32 s24, s0, 0x6000
	s_addc_u32 s25, s1, 0
	s_add_u32 s26, s6, 0x4e000040
	s_addc_u32 s27, s7, 0
	s_and_b32 s94, s64, 1
	s_cmp_eq_u32 s94, 0
	s_cbranch_scc0 .Lstg_pre_l1
	s_mov_b32 m0, s90
	s_nop 0
	global_load_lds_dwordx4 v164, s[24:25]
	s_mov_b32 m0, s88
	s_nop 0
	global_load_lds_dwordx4 v170, s[26:27]
	s_add_u32 s24, s24, 0x3000
	s_addc_u32 s25, s25, 0
	s_add_u32 s26, s26, 64
	s_addc_u32 s27, s27, 0
